# baseline (speedup 1.0000x reference)
.LBB1_2:
	s_load_dwordx8 s[4:11], s[0:1], 0x0
	s_lshr_b32 s0, s2, 3
	s_bfe_u32 s33, s2, 0x30003
	v_readfirstlane_b32 s36, v0
	s_and_b32 s3, s2, 7
	s_and_b32 s0, s0, 8
	s_xor_b32 s44, s33, 15
	s_bfe_u32 s38, s36, 0x20006
	s_or_b32 s14, s0, s3
	s_lshr_b32 s30, s2, 7
	s_mov_b32 s31, 0
	s_lshl_b32 s0, s44, 7
	s_lshl_b32 s39, s38, 5
	s_lshl_b64 s[18:19], s[30:31], 11
	s_or_b32 s0, s39, s0
	s_or_b32 s0, s18, s0
	s_mov_b32 s1, s19
	s_lshr_b32 s35, s36, 6
	s_lshr_b32 s37, s36, 8
	s_lshl_b64 s[12:13], s[0:1], 11
	s_waitcnt lgkmcnt(0)
	s_add_u32 s12, s4, s12
	s_addc_u32 s13, s5, s13
	s_lshl_b32 s42, s14, 6
	s_lshl_b32 s14, s14, 7
	s_add_u32 s16, s12, s14
	s_addc_u32 s17, s13, 0
	s_lshl_b64 s[12:13], s[30:31], 22
	s_add_u32 s6, s6, s12
	s_addc_u32 s7, s7, s13
	s_add_u32 s6, s6, s14
	s_addc_u32 s7, s7, 0
	s_lshr_b32 s15, s36, 4
	v_and_b32_e32 v200, 7, v0
	v_bfe_u32 v208, v0, 4, 2
	s_and_b32 s15, s15, 4
	v_bfe_u32 v193, v0, 3, 3
	v_bitop3_b32 v1, s15, v200, v208 bitop3:0x36
	s_add_u32 s15, s8, s12
	v_lshl_or_b32 v188, s35, 3, v193
	v_mov_b32_e32 v189, 0
	s_addc_u32 s20, s9, s13
	v_lshlrev_b64 v[2:3], 11, v[188:189]
	v_lshlrev_b32_e32 v188, 4, v1
	s_add_u32 s14, s15, s14
	v_lshlrev_b32_e32 v1, 8, v0
	v_lshl_add_u64 v[2:3], s[6:7], 0, v[2:3]
	s_addc_u32 s15, s20, 0
	s_lshl_b32 s34, s38, 14
	v_and_b32_e32 v1, 0x3c00, v1
	v_lshl_add_u64 v[194:195], v[2:3], 0, v[188:189]
	v_or_b32_e32 v2, s34, v1
	s_lshl_b32 s30, s37, 6
	s_lshl_b32 s20, s35, 10
	v_lshlrev_b32_e32 v188, 1, v2
	v_lshlrev_b32_e32 v4, 3, v0
	s_cmp_lg_u32 0, -1
	v_lshl_add_u64 v[2:3], s[14:15], 0, v[188:189]
	v_and_b32_e32 v209, 24, v4
	s_cselect_b32 s21, 0, 0
	v_lshl_add_u64 v[2:3], v[2:3], 0, s[30:31]
	v_lshlrev_b32_e32 v190, 1, v209
	v_mov_b32_e32 v191, v189
	s_add_i32 s41, s20, s21
	s_mov_b32 m0, s41
	s_nop 0
	global_load_lds_dwordx4 v[194:195], off
	s_mov_b64 s[22:23], 0x20000
	v_lshl_add_u64 v[196:197], v[2:3], 0, v[190:191]
	v_lshl_add_u64 v[2:3], v[194:195], 0, s[22:23]
	s_add_i32 s21, s41, 0x2000
	s_mov_b32 m0, s21
	s_nop 0
	global_load_lds_dwordx4 v[2:3], off
	s_add_i32 s40, s41, 0xc000
	s_mov_b32 m0, s40
	s_nop 0
	global_load_lds_dwordx4 v[196:197], off
	v_lshl_add_u64 v[198:199], v[196:197], 0, s[22:23]
	s_add_i32 s24, s40, 0x2000
	s_mov_b32 m0, s24
	s_nop 0
	global_load_lds_dwordx4 v[198:199], off
	s_mov_b64 s[24:25], 0x40000
	v_lshl_add_u64 v[2:3], v[194:195], 0, s[24:25]
	s_add_i32 s26, s41, 0x4000
	s_mov_b32 m0, s26
	s_nop 0
	global_load_lds_dwordx4 v[2:3], off
	s_mov_b64 s[26:27], 0x60000
	v_and_b32_e32 v202, 31, v0
	v_lshl_add_u64 v[2:3], v[194:195], 0, s[26:27]
	v_bfe_u32 v201, v0, 5, 1
	s_add_i32 s28, s41, 0x6000
	s_mov_b32 m0, s28
	s_nop 0
	global_load_lds_dwordx4 v[2:3], off
	v_lshlrev_b32_e32 v2, 10, v202
	v_lshl_or_b32 v2, v201, 3, v2
	v_lshlrev_b32_e32 v216, 1, v2
	global_load_dwordx4 v[144:147], v216, s[16:17]
	global_load_dwordx4 v[140:143], v216, s[16:17] offset:32
	global_load_dwordx4 v[136:139], v216, s[16:17] offset:64
	global_load_dwordx4 v[132:135], v216, s[16:17] offset:96
	s_lshl_b32 s28, s37, 13
	v_lshrrev_b32_e32 v2, 1, v0
	s_add_i32 s30, s28, 0
	v_bitop3_b32 v2, v201, v2, 7 bitop3:0x78
	s_mov_b64 s[28:29], 0x80000
	v_lshlrev_b32_e32 v207, 4, v2
	v_lshl_add_u64 v[2:3], v[194:195], 0, s[28:29]
	s_add_i32 s16, s41, 0x8000
	s_mov_b32 m0, s16
	s_nop 0
	global_load_lds_dwordx4 v[2:3], off
	v_lshlrev_b32_e32 v211, 7, v202
	s_mov_b64 s[16:17], 0xa0000
	v_add_u32_e32 v217, s30, v211
	v_lshl_add_u64 v[2:3], v[194:195], 0, s[16:17]
	s_add_i32 s16, s41, 0xa000
	s_mov_b32 m0, s16
	s_nop 0
	global_load_lds_dwordx4 v[2:3], off
	s_waitcnt vmcnt(6) lgkmcnt(0)
	s_barrier
	v_add_u32_e32 v70, v217, v207
	ds_read_b128 v[2:5], v70
	ds_read_b128 v[18:21], v70 offset:4096
	v_xor_b32_e32 v206, 32, v207
	v_add_u32_e32 v71, v217, v206
	ds_read_b128 v[22:25], v71
	ds_read_b128 v[34:37], v71 offset:4096
	v_xor_b32_e32 v205, 64, v207
	s_waitcnt vmcnt(3) lgkmcnt(3)
	v_mfma_f32_32x32x16_f16 v[2:17], v[2:5], v[144:147], 0
	v_add_u32_e32 v72, v217, v205
	v_xor_b32_e32 v204, 0x60, v207
	v_add_u32_e32 v73, v217, v204
	s_mov_b32 s46, 5
	s_movk_i32 s48, 0x4000
	s_mov_b32 s45, 0x8000
	v_and_b32_e32 v212, 63, v0
	s_waitcnt vmcnt(2) lgkmcnt(1)
	v_mfma_f32_32x32x16_f16 v[2:17], v[22:25], v[140:143], v[2:17]
	v_mfma_f32_32x32x16_f16 v[18:33], v[18:21], v[144:147], 0
	s_waitcnt lgkmcnt(0)
	v_mfma_f32_32x32x16_f16 v[18:33], v[34:37], v[140:143], v[18:33]
	ds_read_b128 v[34:37], v72
	ds_read_b128 v[38:41], v72 offset:4096
	s_waitcnt vmcnt(1) lgkmcnt(1)
	v_mfma_f32_32x32x16_f16 v[2:17], v[34:37], v[136:139], v[2:17]
	s_waitcnt lgkmcnt(0)
	v_mfma_f32_32x32x16_f16 v[18:33], v[38:41], v[136:139], v[18:33]
	ds_read_b128 v[34:37], v73
	ds_read_b128 v[38:41], v73 offset:4096
	s_waitcnt vmcnt(0) lgkmcnt(1)
	v_mfma_f32_32x32x16_f16 v[2:17], v[34:37], v[132:135], v[2:17]
	s_waitcnt lgkmcnt(0)
	v_mfma_f32_32x32x16_f16 v[18:33], v[38:41], v[132:135], v[18:33]
	s_nop 9
	v_max_f32_e64 v35, |v2|, |v2|
	s_nop 0
	v_max_f32_e64 v34, |v18|, |v18|
	v_min_f32_e32 v34, v35, v34
	v_min3_f32 v34, v34, |v3|, |v19|
	v_min3_f32 v34, v34, |v4|, |v20|
	v_min3_f32 v34, v34, |v5|, |v21|
	v_min3_f32 v34, v34, |v6|, |v22|
	v_min3_f32 v34, v34, |v7|, |v23|
	v_min3_f32 v34, v34, |v8|, |v24|
	v_min3_f32 v34, v34, |v9|, |v25|
	v_min3_f32 v34, v34, |v10|, |v26|
	v_min3_f32 v34, v34, |v11|, |v27|
	v_min3_f32 v34, v34, |v12|, |v28|
	v_min3_f32 v34, v34, |v13|, |v29|
	v_min3_f32 v34, v34, |v14|, |v30|
	v_min3_f32 v34, v34, |v15|, |v31|
	v_min3_f32 v34, v34, |v16|, |v32|
	v_min3_f32 v34, v34, |v17|, |v33|
	v_cmp_eq_f32_e32 vcc, 0, v34
	s_cbranch_vccnz .LBB1_114
.LBB1_3:
	v_lshlrev_b32_e32 v34, 5, v208
	v_lshlrev_b32_e32 v203, 2, v201
	v_lshrrev_b32_e32 v35, 2, v0
	v_and_b32_e32 v191, 32, v34
	v_and_or_b32 v35, v35, 3, v203
	v_add_u32_e32 v34, s30, v191
	v_lshlrev_b32_e32 v210, 6, v35
	v_add3_u32 v215, v34, v209, v210
	v_max_f32_e32 v34, v3, v3
	v_max_f32_e32 v35, v2, v2
	v_max_f32_e32 v34, v35, v34
	v_max3_f32 v35, v4, v5, v19
	v_max3_f32 v34, v34, v18, v20
	v_max3_f32 v34, v34, v21, v6
	v_max3_f32 v35, v35, v8, v9
	v_max3_f32 v34, v34, v7, v22
	v_max3_f32 v35, v35, v24, v25
	v_max3_f32 v34, v34, v23, v10
	v_max3_f32 v35, v35, v12, v13
	v_max3_f32 v34, v34, v11, v26
	v_max3_f32 v35, v35, v28, v29
	v_max3_f32 v34, v34, v27, v14
	v_max3_f32 v35, v35, v16, v17
	v_max3_f32 v34, v34, v15, v30
	v_max3_f32 v35, v35, v32, v33
	v_max3_f32 v34, v34, v31, v35
	v_mov_b32_e32 v35, v34
	s_lshl_b64 s[16:17], s[0:1], 10
	s_and_b32 s0, s36, 0x3fffffc0
	v_permlane32_swap_b32_e32 v34, v35
	s_lshl_b32 s0, s0, 2
	v_max_f32_e32 v35, v35, v35
	v_max_f32_e32 v34, v34, v34
	s_add_i32 s0, s0, 0
	v_max_f32_e32 v34, v34, v35
	s_mov_b32 s47, 0x41000000
	s_add_i32 s30, s0, 0x18000
	v_cmp_le_f32_e32 vcc, -4.0, v34
	v_cmp_ge_f32_e64 s[0:1], s47, v34
	v_max_f32_e32 v34, 0xf149f2ca, v34
	s_and_b64 s[0:1], vcc, s[0:1]
	v_cndmask_b32_e64 v192, v34, 0, s[0:1]
	v_add_f32_e64 v2, v2, -v192
	v_exp_f32_e32 v50, v2
	v_add_f32_e64 v2, v18, -v192
	v_exp_f32_e32 v34, v2
	v_add_f32_e64 v2, v3, -v192
	v_exp_f32_e32 v51, v2
	v_add_f32_e64 v2, v19, -v192
	v_exp_f32_e32 v35, v2
	v_add_f32_e64 v2, v4, -v192
	v_exp_f32_e32 v52, v2
	v_add_f32_e64 v2, v20, -v192
	v_exp_f32_e32 v36, v2
	v_add_f32_e64 v2, v5, -v192
	v_exp_f32_e32 v53, v2
	v_add_f32_e64 v2, v21, -v192
	v_exp_f32_e32 v37, v2
	v_add_f32_e64 v2, v6, -v192
	v_exp_f32_e32 v54, v2
	v_add_f32_e64 v2, v22, -v192
	v_exp_f32_e32 v38, v2
	v_add_f32_e64 v2, v7, -v192
	v_exp_f32_e32 v55, v2
	v_add_f32_e64 v2, v23, -v192
	v_exp_f32_e32 v39, v2
	v_add_f32_e64 v2, v8, -v192
	v_exp_f32_e32 v56, v2
	v_add_f32_e64 v2, v24, -v192
	v_exp_f32_e32 v40, v2
	v_add_f32_e64 v2, v9, -v192
	v_exp_f32_e32 v57, v2
	v_add_f32_e64 v2, v25, -v192
	v_exp_f32_e32 v41, v2
	v_add_f32_e64 v2, v10, -v192
	v_exp_f32_e32 v58, v2
	v_add_f32_e64 v2, v26, -v192
	v_exp_f32_e32 v42, v2
	v_add_f32_e64 v2, v11, -v192
	v_exp_f32_e32 v59, v2
	v_add_f32_e64 v2, v27, -v192
	v_exp_f32_e32 v43, v2
	v_add_f32_e64 v2, v12, -v192
	v_exp_f32_e32 v60, v2
	v_add_f32_e64 v2, v28, -v192
	v_exp_f32_e32 v44, v2
	v_add_f32_e64 v2, v13, -v192
	v_exp_f32_e32 v61, v2
	v_add_f32_e64 v2, v29, -v192
	v_exp_f32_e32 v45, v2
	v_add_f32_e64 v2, v14, -v192
	v_exp_f32_e32 v62, v2
	v_add_f32_e64 v2, v30, -v192
	v_exp_f32_e32 v46, v2
	v_add_f32_e64 v2, v15, -v192
	v_exp_f32_e32 v63, v2
	v_add_f32_e64 v2, v31, -v192
	v_exp_f32_e32 v47, v2
	v_add_f32_e64 v2, v16, -v192
	v_exp_f32_e32 v64, v2
	v_add_f32_e64 v2, v32, -v192
	v_exp_f32_e32 v48, v2
	v_add_f32_e64 v2, v17, -v192
	v_exp_f32_e32 v65, v2
	v_add_f32_e64 v2, v33, -v192
	s_waitcnt vmcnt(0) lgkmcnt(0)
	s_barrier
	s_mov_b64 s[0:1], 0xc0000
	v_exp_f32_e32 v49, v2
	v_lshl_add_u64 v[2:3], v[194:195], 0, s[0:1]
	s_mov_b32 m0, s41
	s_nop 0
	global_load_lds_dwordx4 v[2:3], off
	s_mov_b64 s[0:1], 0xe0000
	v_lshl_add_u64 v[2:3], v[194:195], 0, s[0:1]
	s_mov_b32 m0, s21
	s_nop 0
	global_load_lds_dwordx4 v[2:3], off
	s_cmp_lg_u32 0, -1
	s_cselect_b32 s0, 0, 0
	s_add_i32 s0, s0, s20
	v_cmp_neq_f32_e32 vcc, 0, v192
	v_lshl_add_u64 v[2:3], v[196:197], 0, s[24:25]
	s_add_i32 s1, s0, 0x10000
	s_mov_b32 m0, s1
	s_nop 0
	global_load_lds_dwordx4 v[2:3], off
	s_add_i32 s0, s0, 0x12000
	v_lshl_add_u64 v[2:3], v[196:197], 0, s[26:27]
	s_mov_b32 m0, s0
	s_nop 0
	global_load_lds_dwordx4 v[2:3], off
	s_cmp_eq_u64 vcc, 0
	ds_read_b128 v[66:69], v70 offset:16384
	ds_read_b128 v[82:85], v70 offset:20480
	ds_read_b128 v[168:171], v71 offset:16384
	ds_read_b128 v[164:167], v71 offset:20480
	ds_read_b128 v[160:163], v72 offset:16384
	ds_read_b128 v[156:159], v72 offset:20480
	ds_read_b128 v[152:155], v73 offset:16384
	ds_read_b128 v[148:151], v73 offset:20480
	s_cselect_b64 s[20:21], -1, 0
	s_lshr_b32 s43, s36, 2
	s_and_b32 s43, s43, 0x3fffffc0
	s_add_u32 s43, s12, s43
	s_addc_u32 s49, s13, 0
	s_lshl_b32 s2, s2, 4
	v_and_b32_e32 v2, 3, v0
	s_lshl_b32 s3, s3, 7
	s_and_b32 s2, s2, 0x400
	v_lshlrev_b32_e32 v188, 4, v2
	v_add_lshl_u32 v4, s34, v1, 1
	s_or_b32 s34, s2, s3
	v_or_b32_e32 v2, s43, v188
	v_mov_b32_e32 v3, s49
	v_mov_b32_e32 v5, v189
	s_add_u32 s2, s8, s34
	v_lshl_add_u64 v[2:3], v[2:3], 0, v[4:5]
	s_addc_u32 s3, s9, 0
	s_waitcnt vmcnt(4) lgkmcnt(0)
	s_barrier
	v_lshl_add_u64 v[2:3], s[2:3], 0, v[2:3]
	v_mov_b32_e32 v18, v189
	v_mov_b32_e32 v19, v189
	v_lshl_add_u64 v[126:127], v[2:3], 0, s[28:29]
	v_mov_b32_e32 v20, v189
	v_mov_b32_e32 v21, v189
	v_mov_b32_e32 v22, v189
	v_mov_b32_e32 v23, v189
	v_mov_b32_e32 v24, v189
	v_mov_b32_e32 v25, v189
	v_mov_b32_e32 v26, v189
	v_mov_b32_e32 v27, v189
	v_mov_b32_e32 v28, v189
	v_mov_b32_e32 v29, v189
	v_mov_b32_e32 v30, v189
	v_mov_b32_e32 v31, v189
	v_mov_b32_e32 v32, v189
	v_mov_b32_e32 v33, v189
	v_mov_b64_e32 v[2:3], v[18:19]
	v_cmp_gt_u32_e64 s[0:1], 32, v212
	v_lshl_add_u32 v214, v202, 2, s30
	v_lshl_add_u32 v213, v201, 4, s30
	v_mov_b32_e32 v180, 0xff800000
	v_mov_b32_e32 v218, v189
	v_mov_b64_e32 v[4:5], v[20:21]
	v_mov_b64_e32 v[6:7], v[22:23]
	v_mov_b64_e32 v[8:9], v[24:25]
	v_mov_b64_e32 v[10:11], v[26:27]
	v_mov_b64_e32 v[12:13], v[28:29]
	v_mov_b64_e32 v[14:15], v[30:31]
	v_mov_b64_e32 v[16:17], v[32:33]
.LBB1_4:
	v_add_u32_e32 v181, s31, v215
	ds_read_b64_tr_b16 v[172:173], v181 offset:49152
	ds_read_b64_tr_b16 v[174:175], v181 offset:49664
	v_add_f32_e32 v70, v50, v51
	v_add_f32_e32 v70, v52, v70
	v_add_f32_e32 v70, v53, v70
	v_add_f32_e32 v70, v54, v70
	v_add_f32_e32 v86, v55, v70
	s_waitcnt lgkmcnt(9)
	v_mfma_f32_32x32x16_f16 v[66:81], v[66:69], v[144:147], 0
	v_cvt_pk_f16_f32 v128, v50, v51
	v_cvt_pk_f16_f32 v129, v52, v53
	ds_read_b64_tr_b16 v[176:177], v181 offset:53248
	ds_read_b64_tr_b16 v[178:179], v181 offset:53760
	v_add_f32_e32 v50, v56, v86
	s_waitcnt lgkmcnt(10)
	v_mfma_f32_32x32x16_f16 v[82:97], v[82:85], v[144:147], 0
	v_add_f32_e32 v50, v57, v50
	v_add_f32_e32 v50, v58, v50
	v_add_f32_e32 v50, v59, v50
	v_cvt_pk_f16_f32 v130, v54, v55
	v_cvt_pk_f16_f32 v131, v56, v57
	ds_read_b64_tr_b16 v[122:123], v181 offset:50176
	ds_read_b64_tr_b16 v[124:125], v181 offset:50688
	s_waitcnt lgkmcnt(11)
	v_mfma_f32_32x32x16_f16 v[66:81], v[168:171], v[140:143], v[66:81]
	v_add_f32_e32 v50, v60, v50
	v_add_f32_e32 v50, v61, v50
	v_add_f32_e32 v50, v62, v50
	v_add_f32_e32 v50, v63, v50
	v_cvt_pk_f16_f32 v106, v58, v59
	v_cvt_pk_f16_f32 v107, v60, v61
	ds_read_b64_tr_b16 v[118:119], v181 offset:54272
	ds_read_b64_tr_b16 v[120:121], v181 offset:54784
	s_waitcnt lgkmcnt(12)
	v_mfma_f32_32x32x16_f16 v[82:97], v[164:167], v[140:143], v[82:97]
	v_add_f32_e32 v50, v64, v50
	v_add_f32_e32 v50, v65, v50
	v_add_f32_e32 v50, v34, v50
	v_add_f32_e32 v50, v35, v50
	v_cvt_pk_f16_f32 v108, v62, v63
	v_cvt_pk_f16_f32 v109, v64, v65
	ds_read_b64_tr_b16 v[114:115], v181 offset:51200
	ds_read_b64_tr_b16 v[116:117], v181 offset:51712
	s_waitcnt lgkmcnt(13)
	v_mfma_f32_32x32x16_f16 v[66:81], v[160:163], v[136:139], v[66:81]
	v_add_f32_e32 v50, v36, v50
	v_add_f32_e32 v50, v37, v50
	v_add_f32_e32 v50, v38, v50
	v_add_f32_e32 v50, v39, v50
	v_cvt_pk_f16_f32 v102, v34, v35
	v_cvt_pk_f16_f32 v103, v36, v37
	ds_read_b64_tr_b16 v[110:111], v181 offset:55296
	ds_read_b64_tr_b16 v[112:113], v181 offset:55808
	s_waitcnt lgkmcnt(14)
	v_mfma_f32_32x32x16_f16 v[82:97], v[156:159], v[136:139], v[82:97]
	v_add_f32_e32 v34, v40, v50
	v_add_f32_e32 v34, v41, v34
	v_add_f32_e32 v34, v42, v34
	v_add_f32_e32 v34, v43, v34
	v_cvt_pk_f16_f32 v104, v38, v39
	v_cvt_pk_f16_f32 v105, v40, v41
	ds_read_b64_tr_b16 v[156:157], v181 offset:52224
	ds_read_b64_tr_b16 v[158:159], v181 offset:52736
	s_waitcnt lgkmcnt(14)
	v_mfma_f32_32x32x16_f16 v[66:81], v[152:155], v[132:135], v[66:81]
	v_add_f32_e32 v34, v44, v34
	v_add_f32_e32 v34, v45, v34
	v_add_f32_e32 v34, v46, v34
	v_add_f32_e32 v34, v47, v34
	v_cvt_pk_f16_f32 v98, v42, v43
	v_cvt_pk_f16_f32 v99, v44, v45
	ds_read_b64_tr_b16 v[152:153], v181 offset:56320
	ds_read_b64_tr_b16 v[154:155], v181 offset:56832
	v_mfma_f32_32x32x16_f16 v[82:97], v[148:151], v[132:135], v[82:97]
	v_add_f32_e32 v34, v48, v34
	v_add_f32_e32 v34, v49, v34
	v_add_f32_e32 v160, 0, v34
	v_cvt_pk_f16_f32 v100, v46, v47
	v_cvt_pk_f16_f32 v101, v48, v49
	s_add_i32 s49, s33, s46
	s_sub_i32 s3, s49, 17
	s_add_i32 s2, s46, -1
	s_min_i32 s3, s3, s33
	s_cmp_gt_u32 s2, s44
	s_cselect_b32 s2, s3, s2
	s_ashr_i32 s3, s2, 31
	s_lshl_b64 s[2:3], s[2:3], 18
	v_lshl_add_u64 v[34:35], v[194:195], 0, s[2:3]
	s_add_i32 s2, s48, s41
	s_mov_b32 m0, s2
	s_nop 0
	global_load_lds_dwordx4 v[34:35], off
	v_lshl_add_u64 v[34:35], v[34:35], 0, s[22:23]
	s_addk_i32 s2, 0x2000
	s_mov_b32 m0, s2
	s_nop 0
	global_load_lds_dwordx4 v[34:35], off
	s_add_i32 s2, s45, s40
	s_mov_b32 m0, s2
	s_nop 0
	global_load_lds_dwordx4 v[126:127], off
	v_lshl_add_u64 v[34:35], v[126:127], 0, s[22:23]
	s_addk_i32 s2, 0x2000
	s_mov_b32 m0, s2
	s_nop 0
	global_load_lds_dwordx4 v[34:35], off
	s_and_b64 vcc, exec, s[20:21]
	s_mov_b64 s[2:3], -1
	s_cbranch_vccz .LBB1_20
	s_andn2_b64 vcc, exec, s[2:3]
	s_cbranch_vccnz .LBB1_8

.LBB1_11:
	s_add_i32 s2, s45, 0x4000
	s_cmpk_lg_u32 s45, 0x8000
	s_cselect_b32 s43, s2, 0
	v_add_u32_e32 v156, s48, v215
	ds_read_b64_tr_b16 v[118:119], v156 offset:49152
	ds_read_b64_tr_b16 v[120:121], v156 offset:49664
	v_add_f32_e32 v54, v66, v67
	v_add_f32_e32 v54, v68, v54
	v_add_f32_e32 v54, v69, v54
	v_add_f32_e32 v54, v70, v54
	v_add_f32_e32 v38, v71, v54
	s_waitcnt lgkmcnt(9)
	v_mfma_f32_32x32x16_f16 v[50:65], v[50:53], v[144:147], 0
	v_cvt_pk_f16_f32 v128, v66, v67
	v_cvt_pk_f16_f32 v129, v68, v69
	ds_read_b64_tr_b16 v[152:153], v156 offset:53248
	ds_read_b64_tr_b16 v[154:155], v156 offset:53760
	v_add_f32_e32 v66, v72, v38
	s_waitcnt lgkmcnt(10)
	v_mfma_f32_32x32x16_f16 v[34:49], v[34:37], v[144:147], 0
	v_add_f32_e32 v66, v73, v66
	v_add_f32_e32 v66, v74, v66
	v_add_f32_e32 v66, v75, v66
	v_cvt_pk_f16_f32 v130, v70, v71
	v_cvt_pk_f16_f32 v131, v72, v73
	ds_read_b64_tr_b16 v[148:149], v156 offset:50176
	ds_read_b64_tr_b16 v[150:151], v156 offset:50688
	s_waitcnt lgkmcnt(11)
	v_mfma_f32_32x32x16_f16 v[50:65], v[122:125], v[140:143], v[50:65]
	v_add_f32_e32 v66, v76, v66
	v_add_f32_e32 v66, v77, v66
	v_add_f32_e32 v66, v78, v66
	v_add_f32_e32 v66, v79, v66
	v_cvt_pk_f16_f32 v106, v74, v75
	v_cvt_pk_f16_f32 v107, v76, v77
	ds_read_b64_tr_b16 v[122:123], v156 offset:54272
	ds_read_b64_tr_b16 v[124:125], v156 offset:54784
	s_waitcnt lgkmcnt(12)
	v_mfma_f32_32x32x16_f16 v[34:49], v[172:175], v[140:143], v[34:49]
	v_add_f32_e32 v66, v80, v66
	v_add_f32_e32 v66, v81, v66
	v_add_f32_e32 v66, v82, v66
	v_add_f32_e32 v66, v83, v66
	v_cvt_pk_f16_f32 v108, v78, v79
	v_cvt_pk_f16_f32 v109, v80, v81
	ds_read_b64_tr_b16 v[114:115], v156 offset:51200
	ds_read_b64_tr_b16 v[116:117], v156 offset:51712
	s_waitcnt lgkmcnt(13)
	v_mfma_f32_32x32x16_f16 v[50:65], v[176:179], v[136:139], v[50:65]
	v_add_f32_e32 v66, v84, v66
	v_add_f32_e32 v66, v85, v66
	v_add_f32_e32 v66, v86, v66
	v_add_f32_e32 v66, v87, v66
	v_cvt_pk_f16_f32 v102, v82, v83
	v_cvt_pk_f16_f32 v103, v84, v85
	ds_read_b64_tr_b16 v[110:111], v156 offset:55296
	ds_read_b64_tr_b16 v[112:113], v156 offset:55808
	s_waitcnt lgkmcnt(14)
	v_mfma_f32_32x32x16_f16 v[34:49], v[164:167], v[136:139], v[34:49]
	v_add_f32_e32 v82, v88, v66
	v_add_f32_e32 v82, v89, v82
	v_add_f32_e32 v82, v90, v82
	v_add_f32_e32 v82, v91, v82
	v_cvt_pk_f16_f32 v104, v86, v87
	v_cvt_pk_f16_f32 v105, v88, v89
	ds_read_b64_tr_b16 v[172:173], v156 offset:52224
	ds_read_b64_tr_b16 v[174:175], v156 offset:52736
	s_waitcnt lgkmcnt(14)
	v_mfma_f32_32x32x16_f16 v[50:65], v[168:171], v[132:135], v[50:65]
	v_add_f32_e32 v82, v92, v82
	v_add_f32_e32 v82, v93, v82
	v_add_f32_e32 v82, v94, v82
	v_add_f32_e32 v82, v95, v82
	v_cvt_pk_f16_f32 v98, v90, v91
	v_cvt_pk_f16_f32 v99, v92, v93
	ds_read_b64_tr_b16 v[176:177], v156 offset:56320
	ds_read_b64_tr_b16 v[178:179], v156 offset:56832
	v_mfma_f32_32x32x16_f16 v[34:49], v[160:163], v[132:135], v[34:49]
	v_add_f32_e32 v82, v96, v82
	v_add_f32_e32 v82, v97, v82
	v_add_f32_e32 v156, 0, v82
	v_cvt_pk_f16_f32 v100, v94, v95
	v_cvt_pk_f16_f32 v101, v96, v97
	s_add_i32 s49, s49, -16
	s_min_i32 s50, s49, s33
	s_cmp_gt_u32 s46, s44
	s_cselect_b64 s[2:3], -1, 0
	s_and_b64 s[48:49], s[2:3], exec
	s_cselect_b32 s48, s50, s46
	s_ashr_i32 s49, s48, 31
	s_lshl_b64 s[48:49], s[48:49], 18
	v_lshl_add_u64 v[82:83], v[194:195], 0, s[48:49]
	s_add_i32 s48, s45, s41
	s_mov_b32 m0, s48
	s_nop 0
	global_load_lds_dwordx4 v[82:83], off
	v_lshl_add_u64 v[82:83], v[82:83], 0, s[22:23]
	s_addk_i32 s48, 0x2000
	s_mov_b32 m0, s48
	s_nop 0
	global_load_lds_dwordx4 v[82:83], off
	v_lshl_add_u64 v[82:83], v[126:127], 0, s[24:25]
	s_add_i32 s48, s43, s40
	s_mov_b32 m0, s48
	s_nop 0
	global_load_lds_dwordx4 v[82:83], off
	v_lshl_add_u64 v[82:83], v[126:127], 0, s[26:27]
	s_addk_i32 s48, 0x2000
	s_mov_b32 m0, s48
	s_nop 0
	global_load_lds_dwordx4 v[82:83], off
	s_andn2_b64 vcc, exec, s[30:31]
	s_mov_b64 s[30:31], -1
	s_cbranch_vccz .LBB1_24
	s_andn2_b64 vcc, exec, s[30:31]
	s_cbranch_vccnz .LBB1_15

.LBB1_30:
	s_add_i32 s24, s46, -4
	s_cmp_ge_u32 s24, s44
	s_cbranch_scc1 .LBB1_39
	s_xor_b64 s[2:3], s[20:21], -1
	s_add_i32 s22, s24, 1
	v_add_u32_e32 v126, s45, v215
	ds_read_b64_tr_b16 v[122:123], v126 offset:49152
	ds_read_b64_tr_b16 v[124:125], v126 offset:49664
	v_add_f32_e32 v70, v50, v51
	v_add_f32_e32 v70, v52, v70
	v_add_f32_e32 v70, v53, v70
	v_add_f32_e32 v70, v54, v70
	v_add_f32_e32 v86, v55, v70
	s_waitcnt lgkmcnt(9)
	v_mfma_f32_32x32x16_f16 v[66:81], v[66:69], v[144:147], 0
	v_cvt_pk_f16_f32 v128, v50, v51
	v_cvt_pk_f16_f32 v129, v52, v53
	s_mov_b32 s23, 0
	ds_read_b64_tr_b16 v[184:185], v126 offset:53248
	ds_read_b64_tr_b16 v[186:187], v126 offset:53760
	v_add_f32_e32 v50, v56, v86
	s_waitcnt lgkmcnt(10)
	v_mfma_f32_32x32x16_f16 v[82:97], v[82:85], v[144:147], 0
	v_add_f32_e32 v50, v57, v50
	v_add_f32_e32 v50, v58, v50
	v_add_f32_e32 v50, v59, v50
	v_cvt_pk_f16_f32 v130, v54, v55
	v_cvt_pk_f16_f32 v131, v56, v57
	s_nop 0
	ds_read_b64_tr_b16 v[176:177], v126 offset:50176
	ds_read_b64_tr_b16 v[178:179], v126 offset:50688
	s_waitcnt lgkmcnt(11)
	v_mfma_f32_32x32x16_f16 v[66:81], v[168:171], v[140:143], v[66:81]
	v_add_f32_e32 v50, v60, v50
	v_add_f32_e32 v50, v61, v50
	v_add_f32_e32 v50, v62, v50
	v_add_f32_e32 v50, v63, v50
	v_cvt_pk_f16_f32 v106, v58, v59
	v_cvt_pk_f16_f32 v107, v60, v61
	s_nop 0
	ds_read_b64_tr_b16 v[118:119], v126 offset:54272
	ds_read_b64_tr_b16 v[120:121], v126 offset:54784
	s_waitcnt lgkmcnt(12)
	v_mfma_f32_32x32x16_f16 v[82:97], v[164:167], v[140:143], v[82:97]
	v_add_f32_e32 v50, v64, v50
	v_add_f32_e32 v50, v65, v50
	v_add_f32_e32 v50, v34, v50
	v_add_f32_e32 v50, v35, v50
	v_cvt_pk_f16_f32 v108, v62, v63
	v_cvt_pk_f16_f32 v109, v64, v65
	s_nop 0
	ds_read_b64_tr_b16 v[114:115], v126 offset:51200
	ds_read_b64_tr_b16 v[116:117], v126 offset:51712
	s_waitcnt lgkmcnt(13)
	v_mfma_f32_32x32x16_f16 v[66:81], v[160:163], v[136:139], v[66:81]
	v_add_f32_e32 v50, v36, v50
	v_add_f32_e32 v50, v37, v50
	v_add_f32_e32 v50, v38, v50
	v_add_f32_e32 v50, v39, v50
	v_cvt_pk_f16_f32 v102, v34, v35
	v_cvt_pk_f16_f32 v103, v36, v37
	s_nop 0
	ds_read_b64_tr_b16 v[110:111], v126 offset:55296
	ds_read_b64_tr_b16 v[112:113], v126 offset:55808
	s_waitcnt lgkmcnt(14)
	v_mfma_f32_32x32x16_f16 v[82:97], v[156:159], v[136:139], v[82:97]
	v_add_f32_e32 v34, v40, v50
	v_add_f32_e32 v34, v41, v34
	v_add_f32_e32 v34, v42, v34
	v_add_f32_e32 v34, v43, v34
	v_cvt_pk_f16_f32 v104, v38, v39
	v_cvt_pk_f16_f32 v105, v40, v41
	s_nop 0
	ds_read_b64_tr_b16 v[172:173], v126 offset:52224
	ds_read_b64_tr_b16 v[174:175], v126 offset:52736
	s_waitcnt lgkmcnt(14)
	v_mfma_f32_32x32x16_f16 v[66:81], v[152:155], v[132:135], v[66:81]
	v_add_f32_e32 v34, v44, v34
	v_add_f32_e32 v34, v45, v34
	v_add_f32_e32 v34, v46, v34
	v_add_f32_e32 v34, v47, v34
	v_cvt_pk_f16_f32 v98, v42, v43
	v_cvt_pk_f16_f32 v99, v44, v45
	s_nop 0
	ds_read_b64_tr_b16 v[180:181], v126 offset:56320
	ds_read_b64_tr_b16 v[182:183], v126 offset:56832
	v_mfma_f32_32x32x16_f16 v[82:97], v[148:151], v[132:135], v[82:97]
	v_add_f32_e32 v34, v48, v34
	v_add_f32_e32 v34, v49, v34
	v_add_f32_e32 v126, 0, v34
	v_cvt_pk_f16_f32 v100, v46, v47
	v_cvt_pk_f16_f32 v101, v48, v49
	s_nop 0
	s_add_i32 s24, s33, s24
	s_add_i32 s24, s24, -13
	s_min_i32 s24, s24, s33
	s_ashr_i32 s25, s24, 31
	s_lshl_b64 s[24:25], s[24:25], 18
	v_lshl_add_u64 v[34:35], v[194:195], 0, s[24:25]
	s_add_i32 s26, s43, s41
	s_mov_b32 m0, s26
	s_nop 0
	global_load_lds_dwordx4 v[34:35], off
	s_mov_b64 s[24:25], 0x20000
	v_lshl_add_u64 v[34:35], v[34:35], 0, s[24:25]
	s_addk_i32 s26, 0x2000
	s_mov_b32 m0, s26
	s_nop 0
	global_load_lds_dwordx4 v[34:35], off
	s_lshl_b64 s[22:23], s[22:23], 18
	v_lshl_add_u64 v[34:35], v[196:197], 0, s[22:23]
	s_add_i32 s22, s30, s40
	s_mov_b32 m0, s22
	s_nop 0
	global_load_lds_dwordx4 v[34:35], off
	v_lshl_add_u64 v[34:35], v[34:35], 0, s[24:25]
	s_addk_i32 s22, 0x2000
	s_andn2_b64 vcc, exec, s[2:3]
	s_mov_b32 m0, s22
	s_nop 0
	global_load_lds_dwordx4 v[34:35], off
	s_cbranch_vccz .LBB1_120

.LBB1_39:
	s_lshl_b32 s2, s33, 7
	s_or_b32 s2, s39, s2
	s_or_b32 s18, s18, s2
	s_lshl_b64 s[2:3], s[18:19], 11
	s_add_u32 s2, s4, s2
	s_addc_u32 s3, s5, s3
	s_lshl_b32 s22, s42, 1
	s_add_u32 s2, s2, s22
	s_addc_u32 s3, s3, 0
	global_load_dwordx4 v[124:127], v216, s[2:3]
	global_load_dwordx4 v[120:123], v216, s[2:3] offset:32
	global_load_dwordx4 v[116:119], v216, s[2:3] offset:64
	global_load_dwordx4 v[112:115], v216, s[2:3] offset:96
	s_mov_b32 s3, 0
	v_add_u32_e32 v110, s45, v215
	ds_read_b64_tr_b16 v[172:173], v110 offset:49152
	ds_read_b64_tr_b16 v[174:175], v110 offset:49664
	v_add_f32_e32 v70, v50, v51
	v_add_f32_e32 v70, v52, v70
	v_add_f32_e32 v70, v53, v70
	v_add_f32_e32 v70, v54, v70
	v_add_f32_e32 v86, v55, v70
	s_waitcnt lgkmcnt(9)
	v_mfma_f32_32x32x16_f16 v[66:81], v[66:69], v[144:147], 0
	v_cvt_pk_f16_f32 v128, v50, v51
	v_cvt_pk_f16_f32 v129, v52, v53
	s_nop 0
	ds_read_b64_tr_b16 v[176:177], v110 offset:53248
	ds_read_b64_tr_b16 v[178:179], v110 offset:53760
	v_add_f32_e32 v50, v56, v86
	s_waitcnt lgkmcnt(10)
	v_mfma_f32_32x32x16_f16 v[82:97], v[82:85], v[144:147], 0
	v_add_f32_e32 v50, v57, v50
	v_add_f32_e32 v50, v58, v50
	v_add_f32_e32 v50, v59, v50
	v_cvt_pk_f16_f32 v130, v54, v55
	v_cvt_pk_f16_f32 v131, v56, v57
	s_nop 0
	ds_read_b64_tr_b16 v[144:145], v110 offset:50176
	ds_read_b64_tr_b16 v[146:147], v110 offset:50688
	s_waitcnt lgkmcnt(11)
	v_mfma_f32_32x32x16_f16 v[66:81], v[168:171], v[140:143], v[66:81]
	v_add_f32_e32 v50, v60, v50
	v_add_f32_e32 v50, v61, v50
	v_add_f32_e32 v50, v62, v50
	v_add_f32_e32 v50, v63, v50
	v_cvt_pk_f16_f32 v106, v58, v59
	v_cvt_pk_f16_f32 v107, v60, v61
	s_nop 0
	ds_read_b64_tr_b16 v[168:169], v110 offset:54272
	ds_read_b64_tr_b16 v[170:171], v110 offset:54784
	s_waitcnt lgkmcnt(12)
	v_mfma_f32_32x32x16_f16 v[82:97], v[164:167], v[140:143], v[82:97]
	v_add_f32_e32 v50, v64, v50
	v_add_f32_e32 v50, v65, v50
	v_add_f32_e32 v50, v34, v50
	v_add_f32_e32 v50, v35, v50
	v_cvt_pk_f16_f32 v108, v62, v63
	v_cvt_pk_f16_f32 v109, v64, v65
	s_nop 0
	ds_read_b64_tr_b16 v[140:141], v110 offset:51200
	ds_read_b64_tr_b16 v[142:143], v110 offset:51712
	s_waitcnt lgkmcnt(13)
	v_mfma_f32_32x32x16_f16 v[66:81], v[160:163], v[136:139], v[66:81]
	v_add_f32_e32 v50, v36, v50
	v_add_f32_e32 v50, v37, v50
	v_add_f32_e32 v50, v38, v50
	v_add_f32_e32 v50, v39, v50
	v_cvt_pk_f16_f32 v102, v34, v35
	v_cvt_pk_f16_f32 v103, v36, v37
	s_nop 0
	ds_read_b64_tr_b16 v[160:161], v110 offset:55296
	ds_read_b64_tr_b16 v[162:163], v110 offset:55808
	s_waitcnt lgkmcnt(14)
	v_mfma_f32_32x32x16_f16 v[82:97], v[156:159], v[136:139], v[82:97]
	v_add_f32_e32 v34, v40, v50
	v_add_f32_e32 v34, v41, v34
	v_add_f32_e32 v34, v42, v34
	v_add_f32_e32 v34, v43, v34
	v_cvt_pk_f16_f32 v104, v38, v39
	v_cvt_pk_f16_f32 v105, v40, v41
	s_nop 0
	ds_read_b64_tr_b16 v[136:137], v110 offset:52224
	ds_read_b64_tr_b16 v[138:139], v110 offset:52736
	s_waitcnt lgkmcnt(14)
	v_mfma_f32_32x32x16_f16 v[66:81], v[152:155], v[132:135], v[66:81]
	v_add_f32_e32 v34, v44, v34
	v_add_f32_e32 v34, v45, v34
	v_add_f32_e32 v34, v46, v34
	v_add_f32_e32 v34, v47, v34
	v_cvt_pk_f16_f32 v98, v42, v43
	v_cvt_pk_f16_f32 v99, v44, v45
	s_nop 0
	ds_read_b64_tr_b16 v[152:153], v110 offset:56320
	ds_read_b64_tr_b16 v[154:155], v110 offset:56832
	v_mfma_f32_32x32x16_f16 v[82:97], v[148:151], v[132:135], v[82:97]
	v_add_f32_e32 v34, v48, v34
	v_add_f32_e32 v34, v49, v34
	v_add_f32_e32 v34, 0, v34
	v_cvt_pk_f16_f32 v100, v46, v47
	v_cvt_pk_f16_f32 v101, v48, v49
	s_nop 0
	s_min_u32 s2, s33, 2
	s_lshl_b32 s2, s2, 18
	v_lshl_add_u64 v[36:37], v[194:195], 0, s[2:3]
	s_add_i32 s4, s43, s41
	s_mov_b32 m0, s4
	s_nop 0
	global_load_lds_dwordx4 v[36:37], off
	s_mov_b64 s[2:3], 0x20000
	v_lshl_add_u64 v[36:37], v[36:37], 0, s[2:3]
	s_add_i32 s2, s4, 0x2000
	s_mov_b32 m0, s2
	s_nop 0
	global_load_lds_dwordx4 v[36:37], off
	s_add_i32 s2, s30, s40
	s_mov_b32 m0, s2
	s_nop 0
	global_load_lds_dwordx4 v[196:197], off
	s_addk_i32 s2, 0x2000
	s_mov_b32 m0, s2
	s_nop 0
	global_load_lds_dwordx4 v[198:199], off
	s_and_b64 vcc, exec, s[20:21]
	s_cbranch_vccz .LBB1_115

.LBB1_46:
	s_waitcnt vmcnt(4) lgkmcnt(0)
	s_barrier
	v_add_f32_e32 v66, v50, v51
	v_add_u32_e32 v76, s43, v215
	v_add_f32_e32 v66, v52, v66
	ds_read_b64_tr_b16 v[68:69], v76 offset:49152
	ds_read_b64_tr_b16 v[70:71], v76 offset:49664
	v_add_f32_e32 v66, v53, v66
	v_add_f32_e32 v66, v54, v66
	v_add_f32_e32 v66, v55, v66
	v_add_f32_e32 v66, v56, v66
	v_add_f32_e32 v66, v57, v66
	v_cvt_pk_f16_f32 v50, v50, v51
	v_cvt_pk_f16_f32 v51, v52, v53
	v_cvt_pk_f16_f32 v52, v54, v55
	v_cvt_pk_f16_f32 v53, v56, v57
	ds_read_b64_tr_b16 v[54:55], v76 offset:50176
	ds_read_b64_tr_b16 v[56:57], v76 offset:50688
	s_waitcnt lgkmcnt(2)
	v_mfma_f32_32x32x16_f16 v[18:33], v[50:53], v[68:71], v[18:33]
	ds_read_b64_tr_b16 v[68:69], v76 offset:53248
	ds_read_b64_tr_b16 v[70:71], v76 offset:53760
	v_add_f32_e32 v66, v58, v66
	v_add_f32_e32 v66, v59, v66
	v_add_f32_e32 v66, v60, v66
	ds_read_b64_tr_b16 v[72:73], v76 offset:54272
	ds_read_b64_tr_b16 v[74:75], v76 offset:54784
	s_lshl_b32 s2, s38, 13
	s_add_i32 s4, s2, 0
	s_waitcnt lgkmcnt(2)
	v_mfma_f32_32x32x16_f16 v[2:17], v[50:53], v[68:71], v[2:17]
	v_add_f32_e32 v50, v61, v66
	v_add_f32_e32 v50, v62, v50
	v_add_f32_e32 v66, v63, v50
	v_cvt_pk_f16_f32 v50, v58, v59
	v_cvt_pk_f16_f32 v51, v60, v61
	v_cvt_pk_f16_f32 v52, v62, v63
	v_cvt_pk_f16_f32 v53, v64, v65
	s_add_i32 s4, s4, 0x18800
	v_mfma_f32_32x32x16_f16 v[18:33], v[50:53], v[54:57], v[18:33]
	v_add_f32_e32 v54, v64, v66
	v_add_f32_e32 v54, v65, v54
	v_add_f32_e32 v54, v34, v54
	v_add_f32_e32 v54, v35, v54
	v_add_f32_e32 v54, v36, v54
	v_add_f32_e32 v58, v37, v54
	v_cvt_pk_f16_f32 v34, v34, v35
	s_waitcnt lgkmcnt(0)
	v_mfma_f32_32x32x16_f16 v[2:17], v[50:53], v[72:75], v[2:17]
	ds_read_b64_tr_b16 v[50:51], v76 offset:51200
	ds_read_b64_tr_b16 v[52:53], v76 offset:51712
	v_cvt_pk_f16_f32 v35, v36, v37
	v_cvt_pk_f16_f32 v36, v38, v39
	v_cvt_pk_f16_f32 v37, v40, v41
	ds_read_b64_tr_b16 v[54:55], v76 offset:52224
	ds_read_b64_tr_b16 v[56:57], v76 offset:52736
	v_add_f32_e32 v38, v38, v58
	v_add_f32_e32 v38, v39, v38
	s_waitcnt lgkmcnt(2)
	v_mfma_f32_32x32x16_f16 v[18:33], v[34:37], v[50:53], v[18:33]
	ds_read_b64_tr_b16 v[50:51], v76 offset:55296
	ds_read_b64_tr_b16 v[52:53], v76 offset:55808
	v_add_f32_e32 v38, v40, v38
	ds_read_b64_tr_b16 v[58:59], v76 offset:56320
	ds_read_b64_tr_b16 v[60:61], v76 offset:56832
	s_cmp_lg_u32 s37, 1
	v_lshlrev_b32_e32 v196, 4, v212
	s_waitcnt lgkmcnt(2)
	v_mfma_f32_32x32x16_f16 v[2:17], v[34:37], v[50:53], v[2:17]
	v_add_f32_e32 v34, v41, v38
	v_add_f32_e32 v34, v42, v34
	v_add_f32_e32 v38, v43, v34
	v_add_f32_e32 v38, v44, v38
	v_add_f32_e32 v38, v45, v38
	v_cvt_pk_f16_f32 v34, v42, v43
	v_cvt_pk_f16_f32 v35, v44, v45
	v_cvt_pk_f16_f32 v36, v46, v47
	v_cvt_pk_f16_f32 v37, v48, v49
	v_add_f32_e32 v38, v46, v38
	v_mfma_f32_32x32x16_f16 v[18:33], v[34:37], v[54:57], v[18:33]
	v_add_f32_e32 v38, v47, v38
	v_add_f32_e32 v38, v48, v38
	v_add_f32_e32 v38, v49, v38
	v_add_f32_e32 v38, v67, v38
	s_waitcnt lgkmcnt(0)
	v_mfma_f32_32x32x16_f16 v[2:17], v[34:37], v[58:61], v[2:17]
	v_mov_b32_e32 v34, v38
	s_nop 1
	v_permlane32_swap_b32_e32 v38, v34
	v_add_f32_e32 v34, v38, v34
	s_and_saveexec_b64 s[2:3], s[0:1]
	ds_write2_b32 v214, v192, v34 offset1:32
	s_or_b64 exec, exec, s[2:3]
	v_add_u32_e32 v74, s4, v196
	s_cmp_lg_u32 s37, 1
	s_cbranch_scc1 .Lmg1_pub0
	ds_write_b128 v74, v[18:21]
	ds_write_b128 v74, v[22:25] offset:1024
	ds_write_b128 v74, v[26:29] offset:2048
	ds_write_b128 v74, v[30:33] offset:3072
	s_branch .Lmg1_pubd
.Lmg1_pub0:
	ds_write_b128 v74, v[2:5] offset:4096
	ds_write_b128 v74, v[6:9] offset:5120
	ds_write_b128 v74, v[10:13] offset:6144
	ds_write_b128 v74, v[14:17] offset:7168
.Lmg1_pubd:
	s_waitcnt lgkmcnt(0)
	s_barrier
	s_and_b32 s5, s36, 0xc0
	s_lshl_b32 s5, s5, 2
	s_add_i32 s5, s5, 0x18000
	s_cmp_lg_u32 s37, 1
	s_cbranch_scc0 .Lmg1_fac1
	s_and_saveexec_b64 s[2:3], s[0:1]
	v_lshl_add_u32 v68, v202, 2, s5
	v_add_u32_e32 v68, 0x400, v68
	ds_read2_b32 v[66:67], v68 offset1:32
	v_max_f32_e32 v68, v192, v192
	s_waitcnt lgkmcnt(0)
	v_max_f32_e32 v69, v66, v66
	v_max_f32_e32 v68, v68, v69
	v_sub_f32_e32 v69, v192, v68
	v_sub_f32_e32 v70, v66, v68
	v_exp_f32_e32 v70, v70
	v_exp_f32_e32 v69, v69
	v_mul_f32_e32 v67, v67, v70
	v_fmac_f32_e32 v67, v34, v69
	v_rcp_f32_e32 v71, v67
	s_nop 0
	v_mul_f32_e32 v69, v69, v71
	v_mul_f32_e32 v70, v70, v71
	ds_write_b32 v214, v69 offset:51200
	ds_write_b32 v214, v70 offset:51328
	s_or_b64 exec, exec, s[2:3]
	s_branch .Lmg1_facd
.Lmg1_fac1:
	s_and_saveexec_b64 s[2:3], s[0:1]
	v_lshl_add_u32 v68, v202, 2, s5
	ds_read2_b32 v[66:67], v68 offset1:32
	v_max_f32_e32 v69, v192, v192
	s_waitcnt lgkmcnt(0)
	v_max_f32_e32 v68, v66, v66
	v_max_f32_e32 v68, v68, v69
	v_sub_f32_e32 v69, v66, v68
	v_sub_f32_e32 v70, v192, v68
	v_exp_f32_e32 v70, v70
	v_exp_f32_e32 v69, v69
	v_mul_f32_e32 v71, v34, v70
	v_fmac_f32_e32 v71, v67, v69
	v_rcp_f32_e32 v72, v71
	s_nop 0
	v_mul_f32_e32 v69, v69, v72
	v_mul_f32_e32 v70, v70, v72
	ds_write_b32 v214, v69 offset:51200
	ds_write_b32 v214, v70 offset:51328
	s_or_b64 exec, exec, s[2:3]
.Lmg1_facd:
	s_waitcnt lgkmcnt(0)
	ds_read_b128 v[34:37], v213 offset:51200
	ds_read_b128 v[42:45], v213 offset:51328
	ds_read_b128 v[38:41], v213 offset:51232
	ds_read_b128 v[46:49], v213 offset:51360
	ds_read_b128 v[50:53], v213 offset:51264
	ds_read_b128 v[58:61], v213 offset:51392
	ds_read_b128 v[54:57], v213 offset:51296
	ds_read_b128 v[62:65], v213 offset:51424
	s_lshl_b64 s[2:3], s[16:17], 1
	s_add_u32 s2, s10, s2
	s_addc_u32 s3, s11, s3
	s_add_u32 s2, s2, s22
	s_addc_u32 s3, s3, 0
	s_lshl_b32 s4, s38, 12
	s_add_i32 s4, s4, 0x20800
	v_lshlrev_b32_e32 v75, 1, v202
	v_lshl_add_u32 v75, v201, 9, v75
	v_add_u32_e32 v75, s4, v75
	s_cmp_lg_u32 s37, 1
	s_cbranch_scc0 .Lmg1_half1
	ds_read_b128 v[66:69], v74
	ds_read_b128 v[70:73], v74 offset:1024
	ds_read_b128 v[6:9], v74 offset:2048
	ds_read_b128 v[10:13], v74 offset:3072
	s_waitcnt lgkmcnt(0)
	v_mul_f32_e32 v3, v42, v66
	v_fma_mixlo_f16 v3, v18, v34, v3
	ds_write_b16 v75, v3
	v_mul_f32_e32 v3, v43, v67
	v_fma_mixlo_f16 v3, v19, v35, v3
	ds_write_b16 v75, v3 offset:128
	v_mul_f32_e32 v3, v44, v68
	v_fma_mixlo_f16 v3, v20, v36, v3
	ds_write_b16 v75, v3 offset:256
	v_mul_f32_e32 v3, v45, v69
	v_fma_mixlo_f16 v3, v21, v37, v3
	ds_write_b16 v75, v3 offset:384
	v_mul_f32_e32 v3, v46, v70
	v_fma_mixlo_f16 v3, v22, v38, v3
	ds_write_b16 v75, v3 offset:1024
	v_mul_f32_e32 v3, v47, v71
	v_fma_mixlo_f16 v3, v23, v39, v3
	ds_write_b16 v75, v3 offset:1152
	v_mul_f32_e32 v3, v48, v72
	v_fma_mixlo_f16 v3, v24, v40, v3
	ds_write_b16 v75, v3 offset:1280
	v_mul_f32_e32 v3, v49, v73
	v_fma_mixlo_f16 v3, v25, v41, v3
	ds_write_b16 v75, v3 offset:1408
	v_mul_f32_e32 v3, v58, v6
	v_fma_mixlo_f16 v3, v26, v50, v3
	ds_write_b16 v75, v3 offset:2048
	v_mul_f32_e32 v3, v59, v7
	v_fma_mixlo_f16 v3, v27, v51, v3
	ds_write_b16 v75, v3 offset:2176
	v_mul_f32_e32 v3, v60, v8
	v_fma_mixlo_f16 v3, v28, v52, v3
	ds_write_b16 v75, v3 offset:2304
	v_mul_f32_e32 v3, v61, v9
	v_fma_mixlo_f16 v3, v29, v53, v3
	ds_write_b16 v75, v3 offset:2432
	v_mul_f32_e32 v3, v62, v10
	v_fma_mixlo_f16 v3, v30, v54, v3
	ds_write_b16 v75, v3 offset:3072
	v_mul_f32_e32 v3, v63, v11
	v_fma_mixlo_f16 v3, v31, v55, v3
	ds_write_b16 v75, v3 offset:3200
	v_mul_f32_e32 v3, v64, v12
	v_fma_mixlo_f16 v3, v32, v56, v3
	ds_write_b16 v75, v3 offset:3328
	v_mul_f32_e32 v3, v65, v13
	v_fma_mixlo_f16 v3, v33, v57, v3
	ds_write_b16 v75, v3 offset:3456
	v_mov_b32_e32 v71, v193
	v_or_b32_e32 v72, 8, v193
	s_branch .Lmg1_st
.Lmg1_half1:
	ds_read_b128 v[66:69], v74 offset:4096
	ds_read_b128 v[70:73], v74 offset:5120
	ds_read_b128 v[22:25], v74 offset:6144
	ds_read_b128 v[26:29], v74 offset:7168
	s_waitcnt lgkmcnt(0)
	v_mul_f32_e32 v19, v42, v2
	v_fma_mixlo_f16 v19, v66, v34, v19
	ds_write_b16 v75, v19 offset:64
	v_mul_f32_e32 v19, v43, v3
	v_fma_mixlo_f16 v19, v67, v35, v19
	ds_write_b16 v75, v19 offset:192
	v_mul_f32_e32 v19, v44, v4
	v_fma_mixlo_f16 v19, v68, v36, v19
	ds_write_b16 v75, v19 offset:320
	v_mul_f32_e32 v19, v45, v5
	v_fma_mixlo_f16 v19, v69, v37, v19
	ds_write_b16 v75, v19 offset:448
	v_mul_f32_e32 v19, v46, v6
	v_fma_mixlo_f16 v19, v70, v38, v19
	ds_write_b16 v75, v19 offset:1088
	v_mul_f32_e32 v19, v47, v7
	v_fma_mixlo_f16 v19, v71, v39, v19
	ds_write_b16 v75, v19 offset:1216
	v_mul_f32_e32 v19, v48, v8
	v_fma_mixlo_f16 v19, v72, v40, v19
	ds_write_b16 v75, v19 offset:1344
	v_mul_f32_e32 v19, v49, v9
	v_fma_mixlo_f16 v19, v73, v41, v19
	ds_write_b16 v75, v19 offset:1472
	v_mul_f32_e32 v19, v58, v10
	v_fma_mixlo_f16 v19, v22, v50, v19
	ds_write_b16 v75, v19 offset:2112
	v_mul_f32_e32 v19, v59, v11
	v_fma_mixlo_f16 v19, v23, v51, v19
	ds_write_b16 v75, v19 offset:2240
	v_mul_f32_e32 v19, v60, v12
	v_fma_mixlo_f16 v19, v24, v52, v19
	ds_write_b16 v75, v19 offset:2368
	v_mul_f32_e32 v19, v61, v13
	v_fma_mixlo_f16 v19, v25, v53, v19
	ds_write_b16 v75, v19 offset:2496
	v_mul_f32_e32 v19, v62, v14
	v_fma_mixlo_f16 v19, v26, v54, v19
	ds_write_b16 v75, v19 offset:3136
	v_mul_f32_e32 v19, v63, v15
	v_fma_mixlo_f16 v19, v27, v55, v19
	ds_write_b16 v75, v19 offset:3264
	v_mul_f32_e32 v19, v64, v16
	v_fma_mixlo_f16 v19, v28, v56, v19
	ds_write_b16 v75, v19 offset:3392
	v_mul_f32_e32 v19, v65, v17
	v_fma_mixlo_f16 v19, v29, v57, v19
	ds_write_b16 v75, v19 offset:3520
	v_or_b32_e32 v71, 16, v193
	v_or_b32_e32 v72, 24, v193
.Lmg1_st:
	s_waitcnt lgkmcnt(0)
	s_barrier
	v_lshlrev_b32_e32 v66, 4, v200
	v_mov_b32_e32 v67, 0
	v_lshl_add_u64 v[68:69], s[2:3], 0, v[66:67]
	v_add_u32_e32 v70, s4, v66
	v_lshl_add_u32 v73, v71, 7, v70
	v_lshl_add_u32 v74, v72, 7, v70
	ds_read_b128 v[34:37], v73
	ds_read_b128 v[38:41], v74
	v_lshlrev_b32_e32 v66, 11, v71
	v_lshl_add_u64 v[42:43], v[68:69], 0, v[66:67]
	v_lshlrev_b32_e32 v66, 11, v72
	v_lshl_add_u64 v[44:45], v[68:69], 0, v[66:67]
	s_waitcnt lgkmcnt(1)
	global_store_dwordx4 v[42:43], v[34:37], off sc1
	s_nop 1
	s_waitcnt lgkmcnt(0)
	global_store_dwordx4 v[44:45], v[38:41], off sc1
	s_nop 1

.LBB1_57:
	v_add_u32_e32 v0, s2, v191
	v_add3_u32 v197, v0, v209, v210
	v_max_f32_e32 v0, v33, v33
	v_max_f32_e32 v2, v32, v32
	v_max_f32_e32 v0, v2, v0
	v_max3_f32 v2, v34, v35, v17
	v_max3_f32 v0, v0, v16, v18
	v_max3_f32 v0, v0, v19, v36
	v_max3_f32 v2, v2, v38, v39
	v_max3_f32 v0, v0, v37, v20
	v_max3_f32 v2, v2, v22, v23
	v_max3_f32 v0, v0, v21, v40
	v_max3_f32 v2, v2, v42, v43
	v_max3_f32 v0, v0, v41, v24
	v_max3_f32 v2, v2, v26, v27
	v_max3_f32 v0, v0, v25, v44
	v_max3_f32 v2, v2, v46, v47
	v_max3_f32 v0, v0, v45, v28
	v_max3_f32 v2, v2, v30, v31
	v_max3_f32 v0, v0, v29, v2
	v_mov_b32_e32 v2, v0
	s_and_b32 s3, s23, 0x3fffffc0
	s_nop 0
	v_permlane32_swap_b32_e32 v0, v2
	s_lshl_b32 s2, s3, 2
	v_max_f32_e32 v2, v2, v2
	v_max_f32_e32 v0, v0, v0
	s_add_i32 s27, s2, 0
	v_max_f32_e32 v0, v0, v2
	s_mov_b32 s2, 0x41000000
	v_cmp_le_f32_e32 vcc, -4.0, v0
	v_cmp_ge_f32_e64 s[2:3], s2, v0
	v_max_f32_e32 v0, 0xf149f2ca, v0
	s_and_b64 s[2:3], vcc, s[2:3]
	v_cndmask_b32_e64 v192, v0, 0, s[2:3]
	v_add_f32_e64 v0, v32, -v192
	v_exp_f32_e32 v64, v0
	v_add_f32_e64 v0, v16, -v192
	v_exp_f32_e32 v32, v0
	v_add_f32_e64 v0, v33, -v192
	v_exp_f32_e32 v65, v0
	v_add_f32_e64 v0, v17, -v192
	v_exp_f32_e32 v33, v0
	v_add_f32_e64 v0, v34, -v192
	v_exp_f32_e32 v66, v0
	v_add_f32_e64 v0, v18, -v192
	v_exp_f32_e32 v34, v0
	v_add_f32_e64 v0, v35, -v192
	v_exp_f32_e32 v67, v0
	v_add_f32_e64 v0, v19, -v192
	v_exp_f32_e32 v35, v0
	v_add_f32_e64 v0, v36, -v192
	v_exp_f32_e32 v68, v0
	v_add_f32_e64 v0, v20, -v192
	v_exp_f32_e32 v36, v0
	v_add_f32_e64 v0, v37, -v192
	v_exp_f32_e32 v69, v0
	v_add_f32_e64 v0, v21, -v192
	v_exp_f32_e32 v37, v0
	v_add_f32_e64 v0, v38, -v192
	v_exp_f32_e32 v70, v0
	v_add_f32_e64 v0, v22, -v192
	v_exp_f32_e32 v38, v0
	v_add_f32_e64 v0, v39, -v192
	v_exp_f32_e32 v71, v0
	v_add_f32_e64 v0, v23, -v192
	v_exp_f32_e32 v39, v0
	v_add_f32_e64 v0, v40, -v192
	v_exp_f32_e32 v72, v0
	v_add_f32_e64 v0, v24, -v192
	v_exp_f32_e32 v40, v0
	v_add_f32_e64 v0, v41, -v192
	v_exp_f32_e32 v73, v0
	v_add_f32_e64 v0, v25, -v192
	v_exp_f32_e32 v41, v0
	v_add_f32_e64 v0, v42, -v192
	v_exp_f32_e32 v74, v0
	v_add_f32_e64 v0, v26, -v192
	v_exp_f32_e32 v42, v0
	v_add_f32_e64 v0, v43, -v192
	v_exp_f32_e32 v75, v0
	v_add_f32_e64 v0, v27, -v192
	v_exp_f32_e32 v43, v0
	v_add_f32_e64 v0, v44, -v192
	v_exp_f32_e32 v76, v0
	v_add_f32_e64 v0, v28, -v192
	v_exp_f32_e32 v44, v0
	v_add_f32_e64 v0, v45, -v192
	v_exp_f32_e32 v77, v0
	v_add_f32_e64 v0, v29, -v192
	v_exp_f32_e32 v45, v0
	v_add_f32_e64 v0, v46, -v192
	v_exp_f32_e32 v78, v0
	v_add_f32_e64 v0, v30, -v192
	v_exp_f32_e32 v46, v0
	v_add_f32_e64 v0, v47, -v192
	v_exp_f32_e32 v79, v0
	v_add_f32_e64 v0, v31, -v192
	v_exp_f32_e32 v47, v0
	s_waitcnt vmcnt(0) lgkmcnt(0)
	s_barrier
	s_lshr_b32 s26, s23, 6
	s_mov_b32 s5, 0
	s_add_i32 s27, s27, 0x18000
	v_mov_b32_e32 v15, 0
	v_cmp_neq_f32_e64 s[2:3], 0, v192
	s_andn2_b64 vcc, exec, s[16:17]
	s_mov_b32 s18, 1
	s_cbranch_vccnz .LBB1_86
	s_cmp_eq_u64 s[2:3], 0
	s_cselect_b64 s[2:3], -1, 0
	s_lshl_b32 s4, s26, 2
	s_and_b32 s4, s4, 4
	s_lshl_b32 s19, s25, 14
	s_lshl_b32 s29, s26, 10
	s_cmp_lg_u32 0, -1
	v_bitop3_b32 v0, s4, v200, v208 bitop3:0x36
	s_cselect_b32 s4, 0, 0
	v_lshl_or_b32 v48, s26, 3, v193
	v_mov_b32_e32 v49, 0
	v_or_b32_e32 v4, s19, v1
	s_add_i32 s29, s29, s4
	v_lshlrev_b64 v[2:3], 11, v[48:49]
	s_add_i32 s16, s30, 0x4000
	v_lshlrev_b32_e32 v48, 1, v4
	s_lshl_b32 s4, s24, 6
	s_add_i32 s31, s29, 0xc000
	v_lshl_add_u64 v[4:5], s[14:15], 0, v[48:49]
	s_cmpk_lg_u32 s30, 0x8000
	v_lshl_add_u64 v[2:3], s[6:7], 0, v[2:3]
	v_lshl_add_u64 v[4:5], v[4:5], 0, s[4:5]
	v_lshlrev_b32_e32 v48, 4, v0
	s_cselect_b32 s35, s16, 0
	s_min_u32 s4, s33, 3
	v_lshl_add_u64 v[194:195], v[2:3], 0, v[48:49]
	s_lshl_b32 s4, s4, 18
	v_lshl_add_u64 v[2:3], v[194:195], 0, s[4:5]
	s_add_i32 s4, s29, s30
	s_mov_b32 m0, s4
	s_nop 0
	global_load_lds_dwordx4 v[2:3], off
	s_mov_b64 s[6:7], 0x20000
	v_mov_b32_e32 v191, v49
	v_lshl_add_u64 v[2:3], v[2:3], 0, s[6:7]
	s_addk_i32 s4, 0x2000
	s_mov_b32 m0, s4
	s_nop 0
	global_load_lds_dwordx4 v[2:3], off
	v_lshl_add_u64 v[190:191], v[4:5], 0, v[190:191]
	s_mov_b64 s[14:15], 0x40000
	v_lshl_add_u64 v[2:3], v[190:191], 0, s[14:15]
	s_add_i32 s4, s31, s35
	s_mov_b32 m0, s4
	s_nop 0
	global_load_lds_dwordx4 v[2:3], off
	s_mov_b64 s[16:17], 0x60000
	v_lshl_add_u64 v[2:3], v[190:191], 0, s[16:17]
	v_add_u32_e32 v0, s35, v199
	s_addk_i32 s4, 0x2000
	s_mov_b32 m0, s4
	s_nop 0
	global_load_lds_dwordx4 v[2:3], off
	v_add_u32_e32 v2, v0, v207
	ds_read_b128 v[80:83], v2
	ds_read_b128 v[96:99], v2 offset:4096
	v_add_u32_e32 v2, v0, v206
	ds_read_b128 v[164:167], v2
	ds_read_b128 v[160:163], v2 offset:4096
	v_add_u32_e32 v2, v0, v205
	v_add_u32_e32 v0, v0, v204
	ds_read_b128 v[156:159], v2
	ds_read_b128 v[152:155], v2 offset:4096
	ds_read_b128 v[148:151], v0
	ds_read_b128 v[144:147], v0 offset:4096
	s_add_i32 s4, s35, 0x4000
	s_waitcnt vmcnt(4) lgkmcnt(0)
	s_barrier
	s_cmpk_lg_u32 s35, 0x8000
	s_cselect_b32 s28, s4, 0
	s_cmp_lt_u32 s33, 3
	s_cbranch_scc1 .LBB1_87
	s_lshr_b32 s4, s23, 2
	s_and_b32 s4, s4, 0x3fffffc0
	s_add_u32 s20, s12, s4
	s_addc_u32 s21, s13, 0
	v_lshl_add_u64 v[2:3], s[20:21], 0, v[188:189]
	v_add_lshl_u32 v48, s19, v1, 1
	s_add_u32 s8, s8, s34
	v_lshl_add_u64 v[0:1], v[2:3], 0, v[48:49]
	s_addc_u32 s9, s9, 0
	v_lshl_add_u64 v[0:1], s[8:9], 0, v[0:1]
	s_mov_b64 s[8:9], 0x80000
	v_mov_b32_e32 v48, v49
	v_lshl_add_u64 v[180:181], v[0:1], 0, s[8:9]
	v_mov_b32_e32 v50, v49
	v_mov_b32_e32 v51, v49
	v_mov_b32_e32 v52, v49
	v_mov_b32_e32 v53, v49
	v_mov_b32_e32 v54, v49
	v_mov_b32_e32 v55, v49
	v_mov_b32_e32 v56, v49
	v_mov_b32_e32 v57, v49
	v_mov_b32_e32 v58, v49
	v_mov_b32_e32 v59, v49
	v_mov_b32_e32 v60, v49
	v_mov_b32_e32 v61, v49
	v_mov_b32_e32 v62, v49
	v_mov_b32_e32 v63, v49
	v_mov_b64_e32 v[16:17], v[48:49]
	v_mov_b64_e32 v[0:1], v[48:49]
	v_lshl_add_u32 v182, v202, 2, s27
	v_lshl_add_u32 v183, v203, 2, s27
	s_mov_b32 s36, 5
	s_mov_b32 s34, 0x41000000
	v_mov_b32_e32 v184, 0xff800000
	v_mov_b64_e32 v[18:19], v[50:51]
	v_mov_b64_e32 v[20:21], v[52:53]
	v_mov_b64_e32 v[22:23], v[54:55]
	v_mov_b64_e32 v[24:25], v[56:57]
	v_mov_b64_e32 v[26:27], v[58:59]
	v_mov_b64_e32 v[28:29], v[60:61]
	v_mov_b64_e32 v[30:31], v[62:63]
	v_mov_b64_e32 v[2:3], v[50:51]
	v_mov_b64_e32 v[4:5], v[52:53]
	v_mov_b64_e32 v[6:7], v[54:55]
	v_mov_b64_e32 v[8:9], v[56:57]
	v_mov_b64_e32 v[10:11], v[58:59]
	v_mov_b64_e32 v[12:13], v[60:61]
	v_mov_b64_e32 v[14:15], v[62:63]
.LBB1_60:
	v_add_u32_e32 v48, s30, v197
	ds_read_b64_tr_b16 v[172:173], v48 offset:49152
	ds_read_b64_tr_b16 v[174:175], v48 offset:49664
	s_waitcnt lgkmcnt(9)
	v_mfma_f32_32x32x16_f16 v[80:95], v[80:83], v[124:127], 0
	v_add_f32_e32 v50, v64, v65
	v_add_f32_e32 v50, v66, v50
	v_add_f32_e32 v50, v67, v50
	v_add_f32_e32 v50, v68, v50
	v_add_f32_e32 v50, v69, v50
	v_cvt_pk_f16_f32 v140, v64, v65
	v_cvt_pk_f16_f32 v141, v66, v67
	s_nop 0
	ds_read_b64_tr_b16 v[176:177], v48 offset:53248
	ds_read_b64_tr_b16 v[178:179], v48 offset:53760
	s_waitcnt lgkmcnt(10)
	v_mfma_f32_32x32x16_f16 v[96:111], v[96:99], v[124:127], 0
	v_add_f32_e32 v50, v70, v50
	v_add_f32_e32 v50, v71, v50
	v_add_f32_e32 v50, v72, v50
	v_add_f32_e32 v50, v73, v50
	v_cvt_pk_f16_f32 v142, v68, v69
	v_cvt_pk_f16_f32 v143, v70, v71
	s_nop 0
	ds_read_b64_tr_b16 v[168:169], v48 offset:50176
	ds_read_b64_tr_b16 v[170:171], v48 offset:50688
	s_waitcnt lgkmcnt(11)
	v_mfma_f32_32x32x16_f16 v[80:95], v[164:167], v[120:123], v[80:95]
	v_add_f32_e32 v50, v74, v50
	v_add_f32_e32 v50, v75, v50
	v_add_f32_e32 v50, v76, v50
	v_add_f32_e32 v50, v77, v50
	v_cvt_pk_f16_f32 v136, v72, v73
	v_cvt_pk_f16_f32 v137, v74, v75
	s_nop 0
	ds_read_b64_tr_b16 v[164:165], v48 offset:54272
	ds_read_b64_tr_b16 v[166:167], v48 offset:54784
	s_waitcnt lgkmcnt(12)
	v_mfma_f32_32x32x16_f16 v[96:111], v[160:163], v[120:123], v[96:111]
	v_add_f32_e32 v50, v78, v50
	v_add_f32_e32 v50, v79, v50
	v_add_f32_e32 v50, v32, v50
	v_add_f32_e32 v50, v33, v50
	v_cvt_pk_f16_f32 v138, v76, v77
	v_cvt_pk_f16_f32 v139, v78, v79
	s_nop 0
	ds_read_b64_tr_b16 v[70:71], v48 offset:51200
	ds_read_b64_tr_b16 v[72:73], v48 offset:51712
	s_waitcnt lgkmcnt(13)
	v_mfma_f32_32x32x16_f16 v[80:95], v[156:159], v[116:119], v[80:95]
	v_add_f32_e32 v50, v34, v50
	v_add_f32_e32 v50, v35, v50
	v_add_f32_e32 v50, v36, v50
	v_add_f32_e32 v50, v37, v50
	v_cvt_pk_f16_f32 v132, v32, v33
	v_cvt_pk_f16_f32 v133, v34, v35
	s_nop 0
	ds_read_b64_tr_b16 v[66:67], v48 offset:55296
	ds_read_b64_tr_b16 v[68:69], v48 offset:55808
	s_waitcnt lgkmcnt(14)
	v_mfma_f32_32x32x16_f16 v[96:111], v[152:155], v[116:119], v[96:111]
	v_add_f32_e32 v32, v38, v50
	v_add_f32_e32 v32, v39, v32
	v_add_f32_e32 v32, v40, v32
	v_add_f32_e32 v32, v41, v32
	v_cvt_pk_f16_f32 v134, v36, v37
	v_cvt_pk_f16_f32 v135, v38, v39
	s_nop 0
	ds_read_b64_tr_b16 v[74:75], v48 offset:52224
	ds_read_b64_tr_b16 v[76:77], v48 offset:52736
	s_waitcnt lgkmcnt(14)
	v_mfma_f32_32x32x16_f16 v[80:95], v[148:151], v[112:115], v[80:95]
	v_add_f32_e32 v32, v42, v32
	v_add_f32_e32 v32, v43, v32
	v_add_f32_e32 v32, v44, v32
	v_add_f32_e32 v32, v45, v32
	v_cvt_pk_f16_f32 v128, v40, v41
	v_cvt_pk_f16_f32 v129, v42, v43
	s_nop 0
	ds_read_b64_tr_b16 v[148:149], v48 offset:56320
	ds_read_b64_tr_b16 v[150:151], v48 offset:56832
	v_mfma_f32_32x32x16_f16 v[96:111], v[144:147], v[112:115], v[96:111]
	v_add_f32_e32 v32, v46, v32
	v_add_f32_e32 v32, v47, v32
	v_add_f32_e32 v48, 0, v32
	v_cvt_pk_f16_f32 v130, v44, v45
	v_cvt_pk_f16_f32 v131, v46, v47
	s_nop 0
	s_add_i32 s4, s36, -1
	s_min_u32 s4, s4, s33
	s_lshl_b32 s4, s4, 18
	v_lshl_add_u64 v[32:33], v[194:195], 0, s[4:5]
	s_add_i32 s4, s35, s29
	s_mov_b32 m0, s4
	s_nop 0
	global_load_lds_dwordx4 v[32:33], off
	v_lshl_add_u64 v[32:33], v[32:33], 0, s[6:7]
	s_addk_i32 s4, 0x2000
	s_mov_b32 m0, s4
	s_nop 0
	global_load_lds_dwordx4 v[32:33], off
	s_add_i32 s4, s28, s31
	s_mov_b32 m0, s4
	s_nop 0
	global_load_lds_dwordx4 v[180:181], off
	v_lshl_add_u64 v[32:33], v[180:181], 0, s[6:7]
	s_addk_i32 s4, 0x2000
	s_mov_b32 m0, s4
	s_nop 0
	global_load_lds_dwordx4 v[32:33], off
	s_and_b64 vcc, exec, s[2:3]
	s_mov_b64 s[18:19], -1
	s_cbranch_vccz .LBB1_76
	s_andn2_b64 vcc, exec, s[18:19]
	s_cbranch_vccnz .LBB1_64

.LBB1_67:
	s_add_i32 s4, s28, 0x4000
	s_cmpk_lg_u32 s28, 0x8000
	s_cselect_b32 s20, s4, 0
	v_add_u32_e32 v48, s35, v197
	ds_read_b64_tr_b16 v[144:145], v48 offset:49152
	ds_read_b64_tr_b16 v[146:147], v48 offset:49664
	s_waitcnt lgkmcnt(9)
	v_mfma_f32_32x32x16_f16 v[80:95], v[78:81], v[124:127], 0
	v_add_f32_e32 v66, v50, v51
	v_add_f32_e32 v66, v52, v66
	v_add_f32_e32 v66, v53, v66
	v_add_f32_e32 v66, v54, v66
	v_add_f32_e32 v66, v55, v66
	v_cvt_pk_f16_f32 v140, v50, v51
	v_cvt_pk_f16_f32 v141, v52, v53
	s_nop 0
	ds_read_b64_tr_b16 v[152:153], v48 offset:53248
	ds_read_b64_tr_b16 v[154:155], v48 offset:53760
	s_waitcnt lgkmcnt(10)
	v_mfma_f32_32x32x16_f16 v[96:111], v[96:99], v[124:127], 0
	v_add_f32_e32 v50, v56, v66
	v_add_f32_e32 v50, v57, v50
	v_add_f32_e32 v50, v58, v50
	v_add_f32_e32 v50, v59, v50
	v_cvt_pk_f16_f32 v142, v54, v55
	v_cvt_pk_f16_f32 v143, v56, v57
	s_nop 0
	ds_read_b64_tr_b16 v[148:149], v48 offset:50176
	ds_read_b64_tr_b16 v[150:151], v48 offset:50688
	s_waitcnt lgkmcnt(11)
	v_mfma_f32_32x32x16_f16 v[80:95], v[172:175], v[120:123], v[80:95]
	v_add_f32_e32 v50, v60, v50
	v_add_f32_e32 v50, v61, v50
	v_add_f32_e32 v50, v62, v50
	v_add_f32_e32 v50, v63, v50
	v_cvt_pk_f16_f32 v136, v58, v59
	v_cvt_pk_f16_f32 v137, v60, v61
	s_nop 0
	ds_read_b64_tr_b16 v[58:59], v48 offset:54272
	ds_read_b64_tr_b16 v[60:61], v48 offset:54784
	s_waitcnt lgkmcnt(12)
	v_mfma_f32_32x32x16_f16 v[96:111], v[168:171], v[120:123], v[96:111]
	v_add_f32_e32 v50, v64, v50
	v_add_f32_e32 v50, v65, v50
	v_add_f32_e32 v50, v32, v50
	v_add_f32_e32 v50, v33, v50
	v_cvt_pk_f16_f32 v138, v62, v63
	v_cvt_pk_f16_f32 v139, v64, v65
	s_nop 0
	ds_read_b64_tr_b16 v[54:55], v48 offset:51200
	ds_read_b64_tr_b16 v[56:57], v48 offset:51712
	s_waitcnt lgkmcnt(13)
	v_mfma_f32_32x32x16_f16 v[80:95], v[164:167], v[116:119], v[80:95]
	v_add_f32_e32 v50, v34, v50
	v_add_f32_e32 v50, v35, v50
	v_add_f32_e32 v50, v36, v50
	v_add_f32_e32 v62, v37, v50
	v_cvt_pk_f16_f32 v132, v32, v33
	v_cvt_pk_f16_f32 v133, v34, v35
	s_nop 0
	ds_read_b64_tr_b16 v[50:51], v48 offset:55296
	ds_read_b64_tr_b16 v[52:53], v48 offset:55808
	s_waitcnt lgkmcnt(14)
	v_mfma_f32_32x32x16_f16 v[96:111], v[156:159], v[116:119], v[96:111]
	v_add_f32_e32 v32, v38, v62
	v_add_f32_e32 v32, v39, v32
	v_add_f32_e32 v32, v40, v32
	v_add_f32_e32 v32, v41, v32
	v_cvt_pk_f16_f32 v134, v36, v37
	v_cvt_pk_f16_f32 v135, v38, v39
	s_nop 0
	ds_read_b64_tr_b16 v[168:169], v48 offset:52224
	ds_read_b64_tr_b16 v[170:171], v48 offset:52736
	s_waitcnt lgkmcnt(14)
	v_mfma_f32_32x32x16_f16 v[80:95], v[160:163], v[112:115], v[80:95]
	v_add_f32_e32 v32, v42, v32
	v_add_f32_e32 v32, v43, v32
	v_add_f32_e32 v32, v44, v32
	v_add_f32_e32 v32, v45, v32
	v_cvt_pk_f16_f32 v128, v40, v41
	v_cvt_pk_f16_f32 v129, v42, v43
	s_nop 0
	ds_read_b64_tr_b16 v[172:173], v48 offset:56320
	ds_read_b64_tr_b16 v[174:175], v48 offset:56832
	v_mfma_f32_32x32x16_f16 v[96:111], v[70:73], v[112:115], v[96:111]
	v_add_f32_e32 v32, v46, v32
	v_add_f32_e32 v32, v47, v32
	v_add_f32_e32 v48, 0, v32
	v_cvt_pk_f16_f32 v130, v44, v45
	v_cvt_pk_f16_f32 v131, v46, v47
	s_nop 0
	s_min_u32 s4, s36, s33
	s_lshl_b32 s4, s4, 18
	v_lshl_add_u64 v[32:33], v[194:195], 0, s[4:5]
	s_add_i32 s4, s28, s29
	s_mov_b32 m0, s4
	s_nop 0
	global_load_lds_dwordx4 v[32:33], off
	v_lshl_add_u64 v[32:33], v[32:33], 0, s[6:7]
	s_addk_i32 s4, 0x2000
	s_mov_b32 m0, s4
	s_nop 0
	global_load_lds_dwordx4 v[32:33], off
	v_lshl_add_u64 v[32:33], v[180:181], 0, s[14:15]
	s_add_i32 s4, s20, s31
	s_mov_b32 m0, s4
	s_nop 0
	global_load_lds_dwordx4 v[32:33], off
	v_lshl_add_u64 v[32:33], v[180:181], 0, s[16:17]
	s_addk_i32 s4, 0x2000
	s_mov_b32 m0, s4
	s_nop 0
	global_load_lds_dwordx4 v[32:33], off
	s_andn2_b64 vcc, exec, s[18:19]
	s_mov_b64 s[18:19], -1
	s_cbranch_vccz .LBB1_80
	s_andn2_b64 vcc, exec, s[18:19]
	s_cbranch_vccnz .LBB1_71

.LBB1_90:
	s_mov_b64 s[4:5], -1
	s_xor_b64 s[6:7], s[2:3], -1
	v_add_u32_e32 v48, s30, v197
	ds_read_b64_tr_b16 v[54:55], v48 offset:49152
	ds_read_b64_tr_b16 v[56:57], v48 offset:49664
	s_waitcnt lgkmcnt(9)
	v_mfma_f32_32x32x16_f16 v[80:95], v[80:83], v[124:127], 0
	v_add_f32_e32 v50, v64, v65
	v_add_f32_e32 v50, v66, v50
	v_add_f32_e32 v50, v67, v50
	v_add_f32_e32 v50, v68, v50
	v_add_f32_e32 v50, v69, v50
	v_cvt_pk_f16_f32 v140, v64, v65
	v_cvt_pk_f16_f32 v141, v66, v67
	s_mov_b32 s9, 0
	ds_read_b64_tr_b16 v[184:185], v48 offset:53248
	ds_read_b64_tr_b16 v[186:187], v48 offset:53760
	s_waitcnt lgkmcnt(10)
	v_mfma_f32_32x32x16_f16 v[96:111], v[96:99], v[124:127], 0
	v_add_f32_e32 v50, v70, v50
	v_add_f32_e32 v50, v71, v50
	v_add_f32_e32 v50, v72, v50
	v_add_f32_e32 v50, v73, v50
	v_cvt_pk_f16_f32 v142, v68, v69
	v_cvt_pk_f16_f32 v143, v70, v71
	s_nop 0
	ds_read_b64_tr_b16 v[176:177], v48 offset:50176
	ds_read_b64_tr_b16 v[178:179], v48 offset:50688
	s_waitcnt lgkmcnt(11)
	v_mfma_f32_32x32x16_f16 v[80:95], v[164:167], v[120:123], v[80:95]
	v_add_f32_e32 v50, v74, v50
	v_add_f32_e32 v50, v75, v50
	v_add_f32_e32 v50, v76, v50
	v_add_f32_e32 v50, v77, v50
	v_cvt_pk_f16_f32 v136, v72, v73
	v_cvt_pk_f16_f32 v137, v74, v75
	s_nop 0
	ds_read_b64_tr_b16 v[168:169], v48 offset:54272
	ds_read_b64_tr_b16 v[170:171], v48 offset:54784
	s_waitcnt lgkmcnt(12)
	v_mfma_f32_32x32x16_f16 v[96:111], v[160:163], v[120:123], v[96:111]
	v_add_f32_e32 v50, v78, v50
	v_add_f32_e32 v50, v79, v50
	v_add_f32_e32 v50, v32, v50
	v_add_f32_e32 v50, v33, v50
	v_cvt_pk_f16_f32 v138, v76, v77
	v_cvt_pk_f16_f32 v139, v78, v79
	s_nop 0
	ds_read_b64_tr_b16 v[58:59], v48 offset:51200
	ds_read_b64_tr_b16 v[60:61], v48 offset:51712
	s_waitcnt lgkmcnt(13)
	v_mfma_f32_32x32x16_f16 v[80:95], v[156:159], v[116:119], v[80:95]
	v_add_f32_e32 v50, v34, v50
	v_add_f32_e32 v50, v35, v50
	v_add_f32_e32 v50, v36, v50
	v_add_f32_e32 v62, v37, v50
	v_cvt_pk_f16_f32 v132, v32, v33
	v_cvt_pk_f16_f32 v133, v34, v35
	s_nop 0
	ds_read_b64_tr_b16 v[50:51], v48 offset:55296
	ds_read_b64_tr_b16 v[52:53], v48 offset:55808
	s_waitcnt lgkmcnt(14)
	v_mfma_f32_32x32x16_f16 v[96:111], v[152:155], v[116:119], v[96:111]
	v_add_f32_e32 v32, v38, v62
	v_add_f32_e32 v32, v39, v32
	v_add_f32_e32 v32, v40, v32
	v_add_f32_e32 v32, v41, v32
	v_cvt_pk_f16_f32 v134, v36, v37
	v_cvt_pk_f16_f32 v135, v38, v39
	s_nop 0
	ds_read_b64_tr_b16 v[172:173], v48 offset:52224
	ds_read_b64_tr_b16 v[174:175], v48 offset:52736
	s_waitcnt lgkmcnt(14)
	v_mfma_f32_32x32x16_f16 v[80:95], v[148:151], v[112:115], v[80:95]
	v_add_f32_e32 v32, v42, v32
	v_add_f32_e32 v32, v43, v32
	v_add_f32_e32 v32, v44, v32
	v_add_f32_e32 v32, v45, v32
	v_cvt_pk_f16_f32 v128, v40, v41
	v_cvt_pk_f16_f32 v129, v42, v43
	s_nop 0
	ds_read_b64_tr_b16 v[180:181], v48 offset:56320
	ds_read_b64_tr_b16 v[182:183], v48 offset:56832
	v_mfma_f32_32x32x16_f16 v[96:111], v[144:147], v[112:115], v[96:111]
	v_add_f32_e32 v32, v46, v32
	v_add_f32_e32 v32, v47, v32
	v_add_f32_e32 v48, 0, v32
	v_cvt_pk_f16_f32 v130, v44, v45
	v_cvt_pk_f16_f32 v131, v46, v47
	s_nop 0
	s_lshl_b32 s8, s33, 18
	v_lshl_add_u64 v[32:33], v[194:195], 0, s[8:9]
	s_add_i32 s8, s35, s29
	s_mov_b32 m0, s8
	s_nop 0
	global_load_lds_dwordx4 v[32:33], off
	s_mov_b64 s[14:15], 0x20000
	s_addk_i32 s8, 0x2000
	v_lshl_add_u64 v[32:33], v[32:33], 0, s[14:15]
	s_mov_b32 m0, s8
	s_nop 0
	global_load_lds_dwordx4 v[32:33], off
	s_lshl_b32 s8, s18, 18
	v_lshl_add_u64 v[32:33], v[190:191], 0, s[8:9]
	s_mov_b64 s[8:9], 0x40000
	v_lshl_add_u64 v[34:35], v[32:33], 0, s[8:9]
	s_add_i32 s14, s28, s31
	s_mov_b32 m0, s14
	s_nop 0
	global_load_lds_dwordx4 v[34:35], off
	s_mov_b64 s[8:9], 0x60000
	v_lshl_add_u64 v[32:33], v[32:33], 0, s[8:9]
	s_add_i32 s8, s14, 0x2000
	s_andn2_b64 vcc, exec, s[6:7]
	s_mov_b32 m0, s8
	s_nop 0
	global_load_lds_dwordx4 v[32:33], off
	s_cbranch_vccz .LBB1_130
	s_andn2_b64 vcc, exec, s[4:5]
	s_cbranch_vccnz .LBB1_94

.LBB1_105:
	v_add_f32_e32 v48, v64, v65
	s_waitcnt vmcnt(0) lgkmcnt(0)
	s_barrier
	v_add_f32_e32 v48, v66, v48
	v_cvt_pk_f16_f32 v49, v66, v67
	v_add_u32_e32 v66, s28, v197
	ds_read_b64_tr_b16 v[54:55], v66 offset:49152
	ds_read_b64_tr_b16 v[56:57], v66 offset:49664
	v_add_f32_e32 v48, v67, v48
	v_add_f32_e32 v48, v68, v48
	v_add_f32_e32 v48, v69, v48
	v_add_f32_e32 v48, v70, v48
	v_add_f32_e32 v52, v71, v48
	v_cvt_pk_f16_f32 v48, v64, v65
	v_cvt_pk_f16_f32 v50, v68, v69
	v_cvt_pk_f16_f32 v51, v70, v71
	ds_read_b64_tr_b16 v[58:59], v66 offset:50176
	ds_read_b64_tr_b16 v[60:61], v66 offset:50688
	s_waitcnt lgkmcnt(2)
	v_mfma_f32_32x32x16_f16 v[16:31], v[48:51], v[54:57], v[16:31]
	ds_read_b64_tr_b16 v[54:55], v66 offset:53248
	ds_read_b64_tr_b16 v[56:57], v66 offset:53760
	v_add_f32_e32 v52, v72, v52
	v_add_f32_e32 v52, v73, v52
	v_add_f32_e32 v52, v74, v52
	ds_read_b64_tr_b16 v[62:63], v66 offset:54272
	ds_read_b64_tr_b16 v[64:65], v66 offset:54784
	s_lshl_b32 s2, s25, 13
	s_add_i32 s4, s2, 0
	s_waitcnt lgkmcnt(2)
	v_mfma_f32_32x32x16_f16 v[0:15], v[48:51], v[54:57], v[0:15]
	v_add_f32_e32 v48, v75, v52
	v_add_f32_e32 v48, v76, v48
	v_add_f32_e32 v52, v77, v48
	v_cvt_pk_f16_f32 v48, v72, v73
	v_cvt_pk_f16_f32 v49, v74, v75
	v_cvt_pk_f16_f32 v50, v76, v77
	v_cvt_pk_f16_f32 v51, v78, v79
	v_add_f32_e32 v52, v78, v52
	v_mfma_f32_32x32x16_f16 v[16:31], v[48:51], v[58:61], v[16:31]
	v_add_f32_e32 v52, v79, v52
	v_add_f32_e32 v52, v32, v52
	v_add_f32_e32 v52, v33, v52
	v_add_f32_e32 v52, v34, v52
	v_add_f32_e32 v52, v35, v52
	v_cvt_pk_f16_f32 v32, v32, v33
	v_cvt_pk_f16_f32 v33, v34, v35
	s_waitcnt lgkmcnt(0)
	v_mfma_f32_32x32x16_f16 v[0:15], v[48:51], v[62:65], v[0:15]
	ds_read_b64_tr_b16 v[48:49], v66 offset:51200
	ds_read_b64_tr_b16 v[50:51], v66 offset:51712
	v_cvt_pk_f16_f32 v34, v36, v37
	v_cvt_pk_f16_f32 v35, v38, v39
	ds_read_b64_tr_b16 v[54:55], v66 offset:52224
	ds_read_b64_tr_b16 v[56:57], v66 offset:52736
	v_add_f32_e32 v36, v36, v52
	v_add_f32_e32 v36, v37, v36
	v_add_f32_e32 v36, v38, v36
	s_waitcnt lgkmcnt(2)
	v_mfma_f32_32x32x16_f16 v[16:31], v[32:35], v[48:51], v[16:31]
	ds_read_b64_tr_b16 v[48:49], v66 offset:55296
	ds_read_b64_tr_b16 v[50:51], v66 offset:55808
	ds_read_b64_tr_b16 v[58:59], v66 offset:56320
	ds_read_b64_tr_b16 v[60:61], v66 offset:56832
	s_add_i32 s4, s4, 0x18800
	s_cmp_lg_u32 s24, 1
	s_waitcnt lgkmcnt(2)
	v_mfma_f32_32x32x16_f16 v[0:15], v[32:35], v[48:51], v[0:15]
	v_add_f32_e32 v32, v39, v36
	v_add_f32_e32 v32, v40, v32
	v_add_f32_e32 v36, v41, v32
	v_add_f32_e32 v36, v42, v36
	v_add_f32_e32 v36, v43, v36
	v_cvt_pk_f16_f32 v32, v40, v41
	v_cvt_pk_f16_f32 v33, v42, v43
	v_cvt_pk_f16_f32 v34, v44, v45
	v_cvt_pk_f16_f32 v35, v46, v47
	v_add_f32_e32 v36, v44, v36
	v_mfma_f32_32x32x16_f16 v[16:31], v[32:35], v[54:57], v[16:31]
	v_add_f32_e32 v36, v45, v36
	v_add_f32_e32 v36, v46, v36
	v_add_f32_e32 v36, v47, v36
	v_add_f32_e32 v36, v53, v36
	s_waitcnt lgkmcnt(0)
	v_mfma_f32_32x32x16_f16 v[0:15], v[32:35], v[58:61], v[0:15]
	v_mov_b32_e32 v32, v36
	s_nop 1
	v_permlane32_swap_b32_e32 v36, v32
	v_add_f32_e32 v32, v36, v32
	v_lshl_add_u32 v76, v202, 2, s27
	v_lshl_add_u32 v77, v203, 2, s27
	s_and_saveexec_b64 s[2:3], s[0:1]
	ds_write2_b32 v76, v192, v32 offset1:32
	s_or_b64 exec, exec, s[2:3]
	v_add_u32_e32 v74, s4, v196
	s_cmp_lg_u32 s24, 1
	s_cbranch_scc1 .Lmg2_pub0
	ds_write_b128 v74, v[16:19]
	ds_write_b128 v74, v[20:23] offset:1024
	ds_write_b128 v74, v[24:27] offset:2048
	ds_write_b128 v74, v[28:31] offset:3072
	s_branch .Lmg2_pubd
.Lmg2_pub0:
	ds_write_b128 v74, v[0:3] offset:4096
	ds_write_b128 v74, v[4:7] offset:5120
	ds_write_b128 v74, v[8:11] offset:6144
	ds_write_b128 v74, v[12:15] offset:7168
.Lmg2_pubd:
	s_waitcnt lgkmcnt(0)
	s_barrier
	s_and_b32 s5, s23, 0xc0
	s_lshl_b32 s5, s5, 2
	s_add_i32 s5, s5, 0x18000
	s_cmp_lg_u32 s24, 1
	s_cbranch_scc0 .Lmg2_fac1
	s_and_saveexec_b64 s[2:3], s[0:1]
	v_lshl_add_u32 v68, v202, 2, s5
	v_add_u32_e32 v68, 0x400, v68
	ds_read2_b32 v[66:67], v68 offset1:32
	v_max_f32_e32 v68, v192, v192
	s_waitcnt lgkmcnt(0)
	v_max_f32_e32 v69, v66, v66
	v_max_f32_e32 v68, v68, v69
	v_sub_f32_e32 v69, v192, v68
	v_sub_f32_e32 v70, v66, v68
	v_exp_f32_e32 v70, v70
	v_exp_f32_e32 v69, v69
	v_mul_f32_e32 v67, v67, v70
	v_fmac_f32_e32 v67, v32, v69
	v_rcp_f32_e32 v71, v67
	s_nop 0
	v_mul_f32_e32 v69, v69, v71
	v_mul_f32_e32 v70, v70, v71
	ds_write_b32 v76, v69 offset:51200
	ds_write_b32 v76, v70 offset:51328
	s_or_b64 exec, exec, s[2:3]
	s_branch .Lmg2_facd
.Lmg2_fac1:
	s_and_saveexec_b64 s[2:3], s[0:1]
	v_lshl_add_u32 v68, v202, 2, s5
	ds_read2_b32 v[66:67], v68 offset1:32
	v_max_f32_e32 v69, v192, v192
	s_waitcnt lgkmcnt(0)
	v_max_f32_e32 v68, v66, v66
	v_max_f32_e32 v68, v68, v69
	v_sub_f32_e32 v69, v66, v68
	v_sub_f32_e32 v70, v192, v68
	v_exp_f32_e32 v70, v70
	v_exp_f32_e32 v69, v69
	v_mul_f32_e32 v71, v32, v70
	v_fmac_f32_e32 v71, v67, v69
	v_rcp_f32_e32 v72, v71
	s_nop 0
	v_mul_f32_e32 v69, v69, v72
	v_mul_f32_e32 v70, v70, v72
	ds_write_b32 v76, v69 offset:51200
	ds_write_b32 v76, v70 offset:51328
	s_or_b64 exec, exec, s[2:3]
.Lmg2_facd:
	s_waitcnt lgkmcnt(0)
	ds_read_b128 v[34:37], v77 offset:51200
	ds_read_b128 v[42:45], v77 offset:51328
	ds_read_b128 v[38:41], v77 offset:51232
	ds_read_b128 v[46:49], v77 offset:51360
	ds_read_b128 v[50:53], v77 offset:51264
	ds_read_b128 v[58:61], v77 offset:51392
	ds_read_b128 v[54:57], v77 offset:51296
	ds_read_b128 v[62:65], v77 offset:51424
	s_lshl_b32 s5, s33, 18
	s_lshl_b32 s3, s25, 16
	s_or_b32 s5, s5, s3
	s_add_u32 s2, s10, s12
	s_addc_u32 s3, s11, s13
	s_add_u32 s2, s2, s5
	s_addc_u32 s3, s3, 0
	s_add_u32 s2, s2, s22
	s_addc_u32 s3, s3, 0
	s_lshl_b32 s4, s25, 12
	s_add_i32 s4, s4, 0x20800
	v_lshlrev_b32_e32 v75, 1, v202
	v_lshl_add_u32 v75, v201, 9, v75
	v_add_u32_e32 v75, s4, v75
	s_cmp_lg_u32 s24, 1
	s_cbranch_scc0 .Lmg2_half1
	ds_read_b128 v[66:69], v74
	ds_read_b128 v[70:73], v74 offset:1024
	ds_read_b128 v[6:9], v74 offset:2048
	ds_read_b128 v[10:13], v74 offset:3072
	s_waitcnt lgkmcnt(0)
	v_mul_f32_e32 v3, v42, v66
	v_fma_mixlo_f16 v3, v16, v34, v3
	ds_write_b16 v75, v3
	v_mul_f32_e32 v3, v43, v67
	v_fma_mixlo_f16 v3, v17, v35, v3
	ds_write_b16 v75, v3 offset:128
	v_mul_f32_e32 v3, v44, v68
	v_fma_mixlo_f16 v3, v18, v36, v3
	ds_write_b16 v75, v3 offset:256
	v_mul_f32_e32 v3, v45, v69
	v_fma_mixlo_f16 v3, v19, v37, v3
	ds_write_b16 v75, v3 offset:384
	v_mul_f32_e32 v3, v46, v70
	v_fma_mixlo_f16 v3, v20, v38, v3
	ds_write_b16 v75, v3 offset:1024
	v_mul_f32_e32 v3, v47, v71
	v_fma_mixlo_f16 v3, v21, v39, v3
	ds_write_b16 v75, v3 offset:1152
	v_mul_f32_e32 v3, v48, v72
	v_fma_mixlo_f16 v3, v22, v40, v3
	ds_write_b16 v75, v3 offset:1280
	v_mul_f32_e32 v3, v49, v73
	v_fma_mixlo_f16 v3, v23, v41, v3
	ds_write_b16 v75, v3 offset:1408
	v_mul_f32_e32 v3, v58, v6
	v_fma_mixlo_f16 v3, v24, v50, v3
	ds_write_b16 v75, v3 offset:2048
	v_mul_f32_e32 v3, v59, v7
	v_fma_mixlo_f16 v3, v25, v51, v3
	ds_write_b16 v75, v3 offset:2176
	v_mul_f32_e32 v3, v60, v8
	v_fma_mixlo_f16 v3, v26, v52, v3
	ds_write_b16 v75, v3 offset:2304
	v_mul_f32_e32 v3, v61, v9
	v_fma_mixlo_f16 v3, v27, v53, v3
	ds_write_b16 v75, v3 offset:2432
	v_mul_f32_e32 v3, v62, v10
	v_fma_mixlo_f16 v3, v28, v54, v3
	ds_write_b16 v75, v3 offset:3072
	v_mul_f32_e32 v3, v63, v11
	v_fma_mixlo_f16 v3, v29, v55, v3
	ds_write_b16 v75, v3 offset:3200
	v_mul_f32_e32 v3, v64, v12
	v_fma_mixlo_f16 v3, v30, v56, v3
	ds_write_b16 v75, v3 offset:3328
	v_mul_f32_e32 v3, v65, v13
	v_fma_mixlo_f16 v3, v31, v57, v3
	ds_write_b16 v75, v3 offset:3456
	v_mov_b32_e32 v71, v193
	v_or_b32_e32 v72, 8, v193
	s_branch .Lmg2_st
.Lmg2_half1:
	ds_read_b128 v[66:69], v74 offset:4096
	ds_read_b128 v[70:73], v74 offset:5120
	ds_read_b128 v[22:25], v74 offset:6144
	ds_read_b128 v[26:29], v74 offset:7168
	s_waitcnt lgkmcnt(0)
	v_mul_f32_e32 v19, v42, v0
	v_fma_mixlo_f16 v19, v66, v34, v19
	ds_write_b16 v75, v19 offset:64
	v_mul_f32_e32 v19, v43, v1
	v_fma_mixlo_f16 v19, v67, v35, v19
	ds_write_b16 v75, v19 offset:192
	v_mul_f32_e32 v19, v44, v2
	v_fma_mixlo_f16 v19, v68, v36, v19
	ds_write_b16 v75, v19 offset:320
	v_mul_f32_e32 v19, v45, v3
	v_fma_mixlo_f16 v19, v69, v37, v19
	ds_write_b16 v75, v19 offset:448
	v_mul_f32_e32 v19, v46, v4
	v_fma_mixlo_f16 v19, v70, v38, v19
	ds_write_b16 v75, v19 offset:1088
	v_mul_f32_e32 v19, v47, v5
	v_fma_mixlo_f16 v19, v71, v39, v19
	ds_write_b16 v75, v19 offset:1216
	v_mul_f32_e32 v19, v48, v6
	v_fma_mixlo_f16 v19, v72, v40, v19
	ds_write_b16 v75, v19 offset:1344
	v_mul_f32_e32 v19, v49, v7
	v_fma_mixlo_f16 v19, v73, v41, v19
	ds_write_b16 v75, v19 offset:1472
	v_mul_f32_e32 v19, v58, v8
	v_fma_mixlo_f16 v19, v22, v50, v19
	ds_write_b16 v75, v19 offset:2112
	v_mul_f32_e32 v19, v59, v9
	v_fma_mixlo_f16 v19, v23, v51, v19
	ds_write_b16 v75, v19 offset:2240
	v_mul_f32_e32 v19, v60, v10
	v_fma_mixlo_f16 v19, v24, v52, v19
	ds_write_b16 v75, v19 offset:2368
	v_mul_f32_e32 v19, v61, v11
	v_fma_mixlo_f16 v19, v25, v53, v19
	ds_write_b16 v75, v19 offset:2496
	v_mul_f32_e32 v19, v62, v12
	v_fma_mixlo_f16 v19, v26, v54, v19
	ds_write_b16 v75, v19 offset:3136
	v_mul_f32_e32 v19, v63, v13
	v_fma_mixlo_f16 v19, v27, v55, v19
	ds_write_b16 v75, v19 offset:3264
	v_mul_f32_e32 v19, v64, v14
	v_fma_mixlo_f16 v19, v28, v56, v19
	ds_write_b16 v75, v19 offset:3392
	v_mul_f32_e32 v19, v65, v15
	v_fma_mixlo_f16 v19, v29, v57, v19
	ds_write_b16 v75, v19 offset:3520
	v_or_b32_e32 v71, 16, v193
	v_or_b32_e32 v72, 24, v193

.LBB1_135:
	v_mov_b32_e32 v32, 0xff800000
	v_cmp_neq_f32_e32 vcc, 0, v80
	s_nop 1
	v_cndmask_b32_e32 v80, v32, v80, vcc
	v_cmp_neq_f32_e32 vcc, 0, v96
	s_nop 1
	v_cndmask_b32_e32 v96, v32, v96, vcc
	v_cmp_neq_f32_e32 vcc, 0, v81
	s_nop 1
	v_cndmask_b32_e32 v81, v32, v81, vcc
	v_cmp_neq_f32_e32 vcc, 0, v97
	s_nop 1
	v_cndmask_b32_e32 v97, v32, v97, vcc
	v_cmp_neq_f32_e32 vcc, 0, v82
	s_nop 1
	v_cndmask_b32_e32 v82, v32, v82, vcc
	v_cmp_neq_f32_e32 vcc, 0, v98
	s_nop 1
	v_cndmask_b32_e32 v98, v32, v98, vcc
	v_cmp_neq_f32_e32 vcc, 0, v83
	s_nop 1
	v_cndmask_b32_e32 v83, v32, v83, vcc
	v_cmp_neq_f32_e32 vcc, 0, v99
	s_nop 1
	v_cndmask_b32_e32 v99, v32, v99, vcc
	v_cmp_neq_f32_e32 vcc, 0, v84
	s_nop 1
	v_cndmask_b32_e32 v84, v32, v84, vcc
	v_cmp_neq_f32_e32 vcc, 0, v100
	s_nop 1
	v_cndmask_b32_e32 v100, v32, v100, vcc
	v_cmp_neq_f32_e32 vcc, 0, v85
	s_nop 1
	v_cndmask_b32_e32 v85, v32, v85, vcc
	v_cmp_neq_f32_e32 vcc, 0, v101
	s_nop 1
	v_cndmask_b32_e32 v101, v32, v101, vcc
	v_cmp_neq_f32_e32 vcc, 0, v86
	s_nop 1
	v_cndmask_b32_e32 v86, v32, v86, vcc
	v_cmp_neq_f32_e32 vcc, 0, v102
	s_nop 1
	v_cndmask_b32_e32 v102, v32, v102, vcc
	v_cmp_neq_f32_e32 vcc, 0, v87
	s_nop 1
	v_cndmask_b32_e32 v87, v32, v87, vcc
	v_cmp_neq_f32_e32 vcc, 0, v103
	s_nop 1
	v_cndmask_b32_e32 v103, v32, v103, vcc
	v_cmp_neq_f32_e32 vcc, 0, v88
	s_nop 1
	v_cndmask_b32_e32 v88, v32, v88, vcc
	v_cmp_neq_f32_e32 vcc, 0, v104
	s_nop 1
	v_cndmask_b32_e32 v104, v32, v104, vcc
	v_cmp_neq_f32_e32 vcc, 0, v89
	s_nop 1
	v_cndmask_b32_e32 v89, v32, v89, vcc
	v_cmp_neq_f32_e32 vcc, 0, v105
	s_nop 1
	v_cndmask_b32_e32 v105, v32, v105, vcc
	v_cmp_neq_f32_e32 vcc, 0, v90
	s_nop 1
	v_cndmask_b32_e32 v90, v32, v90, vcc
	v_cmp_neq_f32_e32 vcc, 0, v106
	s_nop 1
	v_cndmask_b32_e32 v106, v32, v106, vcc
	v_cmp_neq_f32_e32 vcc, 0, v91
	s_nop 1
	v_cndmask_b32_e32 v91, v32, v91, vcc
	v_cmp_neq_f32_e32 vcc, 0, v107
	s_nop 1
	v_cndmask_b32_e32 v107, v32, v107, vcc
	v_cmp_neq_f32_e32 vcc, 0, v92
	s_nop 1
	v_cndmask_b32_e32 v92, v32, v92, vcc
	v_cmp_neq_f32_e32 vcc, 0, v108
	s_nop 1
	v_cndmask_b32_e32 v108, v32, v108, vcc
	v_cmp_neq_f32_e32 vcc, 0, v93
	s_nop 1
	v_cndmask_b32_e32 v93, v32, v93, vcc
	v_cmp_neq_f32_e32 vcc, 0, v109
	s_nop 1
	v_cndmask_b32_e32 v109, v32, v109, vcc
	v_cmp_neq_f32_e32 vcc, 0, v94
	s_nop 1
	v_cndmask_b32_e32 v94, v32, v94, vcc
	v_cmp_neq_f32_e32 vcc, 0, v110
	s_nop 1
	v_cndmask_b32_e32 v110, v32, v110, vcc
	v_cmp_neq_f32_e32 vcc, 0, v95
	s_nop 1
	v_cndmask_b32_e32 v95, v32, v95, vcc
	v_cmp_neq_f32_e32 vcc, 0, v111
	s_nop 1
	v_cndmask_b32_e32 v111, v32, v111, vcc
	s_branch .LBB1_93
	s_nop 0
	s_nop 0
	s_nop 0
	s_nop 0
	s_nop 0
	s_nop 0
	s_nop 0
	s_nop 0
	s_endpgm

	.amdhsa_kernel _Z10attn64_fwdPKDF16_S0_S0_PDF16_
		.amdhsa_group_segment_fixed_size 2048
		.amdhsa_private_segment_fixed_size 0
		.amdhsa_kernarg_size 32
		.amdhsa_user_sgpr_count 2
		.amdhsa_user_sgpr_dispatch_ptr 0
		.amdhsa_user_sgpr_queue_ptr 0
		.amdhsa_user_sgpr_kernarg_segment_ptr 1
		.amdhsa_user_sgpr_dispatch_id 0
		.amdhsa_user_sgpr_kernarg_preload_length 0
		.amdhsa_user_sgpr_kernarg_preload_offset 0
		.amdhsa_user_sgpr_private_segment_size 0
		.amdhsa_uses_dynamic_stack 0
		.amdhsa_enable_private_segment 0
		.amdhsa_system_sgpr_workgroup_id_x 1
		.amdhsa_system_sgpr_workgroup_id_y 0
		.amdhsa_system_sgpr_workgroup_id_z 0
		.amdhsa_system_sgpr_workgroup_info 0
		.amdhsa_system_vgpr_workitem_id 0
		.amdhsa_next_free_vgpr 219
		.amdhsa_next_free_sgpr 51
		.amdhsa_accum_offset 220
		.amdhsa_reserve_vcc 1
		.amdhsa_float_round_mode_32 0
		.amdhsa_float_round_mode_16_64 0
		.amdhsa_float_denorm_mode_32 3
		.amdhsa_float_denorm_mode_16_64 3
		.amdhsa_dx10_clamp 1
		.amdhsa_ieee_mode 1
		.amdhsa_fp16_overflow 0
		.amdhsa_tg_split 0
		.amdhsa_exception_fp_ieee_invalid_op 0
		.amdhsa_exception_fp_denorm_src 0
		.amdhsa_exception_fp_ieee_div_zero 0
		.amdhsa_exception_fp_ieee_overflow 0
		.amdhsa_exception_fp_ieee_underflow 0
		.amdhsa_exception_fp_ieee_inexact 0
		.amdhsa_exception_int_div_zero 0
	.end_amdhsa_kernel

.LBB3_2:
	s_load_dword s0, s[0:1], 0x20
	s_and_b32 s14, s2, 7
	v_cvt_f32_ubyte0_e32 v3, s14
	v_lshlrev_b32_e32 v100, 4, v0
	s_mov_b64 s[18:19], 0x20080
	s_waitcnt lgkmcnt(0)
	s_ashr_i32 s1, s0, 31
	s_lshr_b32 s1, s1, 22
	s_add_i32 s1, s0, s1
	s_ashr_i32 s3, s1, 10
	v_cvt_f32_i32_e32 v1, s3
	s_ashr_i32 s1, s1, 31
	s_or_b32 s1, s1, 1
	s_movk_i32 s17, 0x70
	v_rcp_iflag_f32_e32 v2, v1
	s_nop 0
	v_mul_f32_e32 v2, v3, v2
	v_trunc_f32_e32 v2, v2
	v_fma_f32 v3, -v2, v1, v3
	v_cvt_i32_f32_e32 v2, v2
	v_cmp_ge_f32_e64 s[12:13], |v3|, |v1|
	s_and_b64 s[12:13], s[12:13], exec
	s_cselect_b32 s1, s1, 0
	v_readfirstlane_b32 s13, v2
	s_add_i32 s1, s13, s1
	s_lshl_b32 s12, s2, 4
	s_bfe_i32 s13, s1, 0x160000
	s_mul_i32 s1, s1, s3
	s_and_b32 s12, s12, 0x180
	s_sub_i32 s3, s14, s1
	s_lshl_b32 s1, s13, 9
	s_or_b32 s1, s1, s12
	s_lshl_b32 s2, s2, 2
	v_lshrrev_b32_e32 v1, 3, v0
	v_lshrrev_b32_e32 v2, 4, v0
	s_lshl_b32 s3, s3, 10
	s_and_b32 s2, s2, 0xffffff80
	v_xor_b32_e32 v10, v2, v0
	v_or_b32_e32 v2, s1, v1
	s_add_i32 s2, s3, s2
	v_ashrrev_i32_e32 v3, 31, v2
	v_lshlrev_b64 v[4:5], 11, v[2:3]
	v_or_b32_e32 v2, s2, v1
	v_mov_b32_e32 v3, 0
	v_lshlrev_b32_e32 v1, 4, v10
	v_lshlrev_b64 v[6:7], 11, v[2:3]
	v_and_b32_e32 v2, 0x70, v1
	v_add_u32_e32 v1, 0, v100
	v_lshl_add_u64 v[8:9], s[6:7], 0, v[6:7]
	v_lshl_add_u64 v[4:5], s[4:5], 0, v[4:5]
	v_readfirstlane_b32 s6, v1
	v_add_u32_e32 v10, 0x2000, v1
	v_lshl_add_u64 v[6:7], v[4:5], 0, v[2:3]
	v_lshl_add_u64 v[4:5], v[8:9], 0, v[2:3]
	v_add_u32_e32 v2, 0x4000, v1
	s_mov_b32 m0, s6
	s_mov_b64 s[12:13], 0x20000
	v_readfirstlane_b32 s3, v10
	global_load_lds_dwordx4 v[6:7], off
	v_lshl_add_u64 v[8:9], v[6:7], 0, s[12:13]
	s_mov_b32 m0, s3
	v_readfirstlane_b32 s4, v2
	v_add_u32_e32 v2, 0x6000, v1
	global_load_lds_dwordx4 v[8:9], off
	s_mov_b32 m0, s4
	v_readfirstlane_b32 s5, v2
	v_add_u32_e32 v12, 0x8000, v1
	global_load_lds_dwordx4 v[4:5], off
	v_lshl_add_u64 v[8:9], v[4:5], 0, s[12:13]
	s_mov_b32 m0, s5
	s_mov_b64 s[12:13], 0x80
	v_readfirstlane_b32 s16, v12
	v_add_u32_e32 v12, 0xa000, v1
	global_load_lds_dwordx4 v[8:9], off
	v_lshl_add_u64 v[8:9], v[4:5], 0, s[12:13]
	v_add_u32_e32 v2, 0xc000, v1
	v_lshl_add_u64 v[10:11], v[6:7], 0, s[12:13]
	s_mov_b32 m0, s16
	v_readfirstlane_b32 s13, v12
	global_load_lds_dwordx4 v[10:11], off
	v_lshl_add_u64 v[10:11], v[6:7], 0, s[18:19]
	s_mov_b32 m0, s13
	v_readfirstlane_b32 s14, v2
	v_add_u32_e32 v2, 0xe000, v1
	global_load_lds_dwordx4 v[10:11], off
	s_mov_b32 m0, s14
	v_readfirstlane_b32 s15, v2
	s_add_i32 s7, 0, 0x14000
	v_add_u32_e32 v12, 0x10000, v1
	global_load_lds_dwordx4 v[8:9], off
	v_lshl_add_u64 v[8:9], v[4:5], 0, s[18:19]
	s_mov_b32 m0, s15
	s_mov_b64 s[18:19], 0x100
	v_add_u32_e32 v2, s7, v100
	v_readfirstlane_b32 s7, v12
	v_add_u32_e32 v1, 0x12000, v1
	global_load_lds_dwordx4 v[8:9], off
	v_lshl_add_u64 v[8:9], v[4:5], 0, s[18:19]
	v_lshl_add_u64 v[10:11], v[6:7], 0, s[18:19]
	s_mov_b32 m0, s7
	s_mov_b64 s[18:19], 0x20100
	v_readfirstlane_b32 s7, v1
	global_load_lds_dwordx4 v[10:11], off
	v_lshl_add_u64 v[10:11], v[6:7], 0, s[18:19]
	s_mov_b32 m0, s7
	v_readfirstlane_b32 s7, v2
	v_add_u32_e32 v1, 0x2000, v2
	global_load_lds_dwordx4 v[10:11], off
	s_mov_b32 m0, s7
	v_readfirstlane_b32 s12, v1
	global_load_lds_dwordx4 v[8:9], off
	v_lshl_add_u64 v[8:9], v[4:5], 0, s[18:19]
	s_mov_b32 m0, s12
	v_lshrrev_b32_e32 v1, 2, v0
	global_load_lds_dwordx4 v[8:9], off
	v_and_b32_e32 v8, 15, v0
	v_and_b32_e32 v1, 0x60, v1
	v_or_b32_e32 v10, v1, v8
	v_lshlrev_b32_e32 v101, 7, v10
	v_lshlrev_b32_e32 v10, 7, v0
	v_and_b32_e32 v2, 63, v0
	v_lshlrev_b32_e32 v9, 3, v0
	v_and_b32_e32 v102, 0x2780, v10
	v_bitop3_b32 v10, v2, s17, v9 bitop3:0x48
	v_add_u32_e32 v56, 0, v102
	v_add_u32_e32 v48, 0, v101
	s_waitcnt vmcnt(8) lgkmcnt(0)
	s_barrier
	v_add_u32_e32 v2, v56, v10
	v_add_u32_e32 v11, v48, v10
	v_bitop3_b32 v9, v0, v9, 63 bitop3:0x6c
	v_mov_b32_e32 v10, 0x70
	ds_read_b128 v[12:15], v2 offset:16384
	ds_read_b128 v[16:19], v2 offset:18432
	ds_read_b128 v[20:23], v11
	ds_read_b128 v[24:27], v11 offset:2048
	ds_read_b128 v[32:35], v2 offset:20480
	ds_read_b128 v[40:43], v2 offset:22528
	v_bitop3_b32 v103, v9, 64, v10 bitop3:0x6c
	v_add_u32_e32 v10, v48, v103
	v_add_u32_e32 v9, v56, v103
	ds_read_b128 v[48:51], v10
	ds_read_b128 v[52:55], v10 offset:2048
	ds_read_b128 v[56:59], v9 offset:16384
	ds_read_b128 v[60:63], v9 offset:18432
	ds_read_b128 v[64:67], v9 offset:20480
	ds_read_b128 v[68:71], v9 offset:22528
	s_waitcnt lgkmcnt(6)
	v_mfma_f32_16x16x32_f16 v[28:31], v[12:15], v[20:23], 0
	v_mfma_f32_16x16x32_f16 v[36:39], v[16:19], v[20:23], 0
	v_mfma_f32_16x16x32_f16 v[44:47], v[32:35], v[20:23], 0
	v_mfma_f32_16x16x32_f16 v[20:23], v[40:43], v[20:23], 0
	v_mfma_f32_16x16x32_f16 v[12:15], v[12:15], v[24:27], 0
	v_mfma_f32_16x16x32_f16 v[16:19], v[16:19], v[24:27], 0
	v_mfma_f32_16x16x32_f16 v[32:35], v[32:35], v[24:27], 0
	v_mfma_f32_16x16x32_f16 v[24:27], v[40:43], v[24:27], 0
	s_mov_b64 s[18:19], 0x180
	s_mov_b32 m0, s6
	s_waitcnt vmcnt(4) lgkmcnt(0)
	s_barrier
	v_mfma_f32_16x16x32_f16 v[28:31], v[56:59], v[48:51], v[28:31]
	v_lshl_add_u64 v[40:41], v[4:5], 0, s[18:19]
	v_lshl_add_u64 v[42:43], v[6:7], 0, s[18:19]
	s_mov_b64 s[18:19], 0x20180
	global_load_lds_dwordx4 v[42:43], off
	v_mfma_f32_16x16x32_f16 v[36:39], v[60:63], v[48:51], v[36:39]
	v_lshl_add_u64 v[42:43], v[6:7], 0, s[18:19]
	s_mov_b32 m0, s3
	s_nop 0
	global_load_lds_dwordx4 v[42:43], off
	v_mfma_f32_16x16x32_f16 v[44:47], v[64:67], v[48:51], v[44:47]
	s_mov_b32 m0, s4
	s_nop 0
	global_load_lds_dwordx4 v[40:41], off
	v_mfma_f32_16x16x32_f16 v[20:23], v[68:71], v[48:51], v[20:23]
	v_lshl_add_u64 v[40:41], v[4:5], 0, s[18:19]
	s_mov_b32 m0, s5
	s_nop 0
	global_load_lds_dwordx4 v[40:41], off
	ds_read_b128 v[40:43], v11 offset:32768
	ds_read_b128 v[72:75], v11 offset:34816
	ds_read_b128 v[76:79], v2 offset:49152
	ds_read_b128 v[80:83], v2 offset:51200
	ds_read_b128 v[84:87], v2 offset:53248
	ds_read_b128 v[88:91], v2 offset:55296
	v_mfma_f32_16x16x32_f16 v[12:15], v[56:59], v[52:55], v[12:15]
	v_mfma_f32_16x16x32_f16 v[16:19], v[60:63], v[52:55], v[16:19]
	v_mfma_f32_16x16x32_f16 v[32:35], v[64:67], v[52:55], v[32:35]
	v_mfma_f32_16x16x32_f16 v[24:27], v[68:71], v[52:55], v[24:27]
	s_waitcnt lgkmcnt(0)
	v_mfma_f32_16x16x32_f16 v[28:31], v[76:79], v[40:43], v[28:31]
	ds_read_b128 v[52:55], v10 offset:32768
	ds_read_b128 v[56:59], v10 offset:34816
	v_mfma_f32_16x16x32_f16 v[36:39], v[80:83], v[40:43], v[36:39]
	v_mfma_f32_16x16x32_f16 v[44:47], v[84:87], v[40:43], v[44:47]
	v_mfma_f32_16x16x32_f16 v[20:23], v[88:91], v[40:43], v[20:23]
	v_mfma_f32_16x16x32_f16 v[40:43], v[76:79], v[72:75], v[12:15]
	ds_read_b128 v[60:63], v9 offset:49152
	ds_read_b128 v[64:67], v9 offset:51200
	ds_read_b128 v[68:71], v9 offset:53248
	ds_read_b128 v[76:79], v9 offset:55296
	v_mfma_f32_16x16x32_f16 v[48:51], v[80:83], v[72:75], v[16:19]
	v_mfma_f32_16x16x32_f16 v[32:35], v[84:87], v[72:75], v[32:35]
	v_mfma_f32_16x16x32_f16 v[24:27], v[88:91], v[72:75], v[24:27]
	s_mov_b64 s[18:19], 0x200
	s_mov_b32 m0, s16
	s_waitcnt vmcnt(4) lgkmcnt(0)
	s_barrier
	v_mfma_f32_16x16x32_f16 v[28:31], v[60:63], v[52:55], v[28:31]
	v_lshl_add_u64 v[12:13], v[4:5], 0, s[18:19]
	v_lshl_add_u64 v[14:15], v[6:7], 0, s[18:19]
	s_mov_b64 s[18:19], 0x20200
	global_load_lds_dwordx4 v[14:15], off
	v_mfma_f32_16x16x32_f16 v[36:39], v[64:67], v[52:55], v[36:39]
	v_lshl_add_u64 v[14:15], v[6:7], 0, s[18:19]
	s_mov_b32 m0, s13
	v_add_u32_e32 v16, 0x15000, v2
	global_load_lds_dwordx4 v[14:15], off
	v_mfma_f32_16x16x32_f16 v[44:47], v[68:71], v[52:55], v[44:47]
	s_mov_b32 m0, s14
	v_add_u32_e32 v14, 0x14000, v2
	global_load_lds_dwordx4 v[12:13], off
	v_mfma_f32_16x16x32_f16 v[18:21], v[76:79], v[52:55], v[20:23]
	v_lshl_add_u64 v[12:13], v[4:5], 0, s[18:19]
	s_mov_b32 m0, s15
	v_add_u32_e32 v15, 0x14800, v2
	global_load_lds_dwordx4 v[12:13], off
	v_add_u32_e32 v12, 0x10000, v11
	v_add_u32_e32 v13, 0x10800, v11
	ds_read_b128 v[72:75], v12
	ds_read_b128 v[80:83], v13
	ds_read_b128 v[84:87], v14
	ds_read_b128 v[88:91], v15
	v_add_u32_e32 v17, 0x15800, v2
	ds_read_b128 v[92:95], v16
	ds_read_b128 v[96:99], v17
	v_mfma_f32_16x16x32_f16 v[40:43], v[60:63], v[56:59], v[40:43]
	v_mfma_f32_16x16x32_f16 v[48:51], v[64:67], v[56:59], v[48:51]
	v_mfma_f32_16x16x32_f16 v[32:35], v[68:71], v[56:59], v[32:35]
	v_mfma_f32_16x16x32_f16 v[22:25], v[76:79], v[56:59], v[24:27]
	s_add_i32 s17, 0, 0x10000
	s_waitcnt lgkmcnt(0)
	v_mfma_f32_16x16x32_f16 v[52:55], v[96:99], v[72:75], v[18:21]
	s_nop 2
	v_add_u32_e32 v18, s17, v103
	v_add_u32_e32 v19, v18, v101
	v_add_u32_e32 v18, v18, v102
	v_mfma_f32_16x16x32_f16 v[26:29], v[84:87], v[72:75], v[28:31]
	ds_read_b128 v[56:59], v19
	ds_read_b128 v[60:63], v19 offset:2048
	v_mfma_f32_16x16x32_f16 v[36:39], v[88:91], v[72:75], v[36:39]
	v_mfma_f32_16x16x32_f16 v[44:47], v[92:95], v[72:75], v[44:47]
	ds_read_b128 v[64:67], v18 offset:16384
	ds_read_b128 v[68:71], v18 offset:18432
	ds_read_b128 v[72:75], v18 offset:20480
	ds_read_b128 v[76:79], v18 offset:22528
	v_mfma_f32_16x16x32_f16 v[40:43], v[84:87], v[80:83], v[40:43]
	v_mfma_f32_16x16x32_f16 v[48:51], v[88:91], v[80:83], v[48:51]
	v_mfma_f32_16x16x32_f16 v[30:33], v[92:95], v[80:83], v[32:35]
	v_mfma_f32_16x16x32_f16 v[20:23], v[96:99], v[80:83], v[22:25]
	s_mov_b64 s[18:19], 0x280
	v_add_u32_e32 v80, s17, v100
	s_nop 0
	v_lshl_add_u64 v[24:25], v[4:5], 0, s[18:19]
	v_lshl_add_u64 v[34:35], v[6:7], 0, s[18:19]
	v_readfirstlane_b32 s18, v80
	v_add_u32_e32 v80, 0x2000, v80
	s_waitcnt vmcnt(4) lgkmcnt(0)
	s_barrier
	s_mov_b32 m0, s18
	s_mov_b64 s[20:21], 0x20280
	v_readfirstlane_b32 s17, v80
	global_load_lds_dwordx4 v[34:35], off
	v_lshl_add_u64 v[34:35], v[6:7], 0, s[20:21]
	s_mov_b32 m0, s17
	s_nop 0
	global_load_lds_dwordx4 v[34:35], off
	s_mov_b32 m0, s7
	s_nop 0
	global_load_lds_dwordx4 v[24:25], off
	v_lshl_add_u64 v[24:25], v[4:5], 0, s[20:21]
	s_mov_b32 m0, s12
	s_nop 0
	global_load_lds_dwordx4 v[24:25], off
	v_mfma_f32_16x16x32_f16 v[24:27], v[64:67], v[56:59], v[26:29]
	v_mfma_f32_16x16x32_f16 v[34:37], v[68:71], v[56:59], v[36:39]
	v_mfma_f32_16x16x32_f16 v[44:47], v[72:75], v[56:59], v[44:47]
	v_mfma_f32_16x16x32_f16 v[52:55], v[76:79], v[56:59], v[52:55]
	ds_read_b128 v[80:83], v11
	ds_read_b128 v[84:87], v11 offset:2048
	ds_read_b128 v[88:91], v2 offset:16384
	ds_read_b128 v[92:95], v2 offset:18432
	ds_read_b128 v[96:99], v2 offset:20480
	ds_read_b128 v[100:103], v2 offset:22528
	v_mfma_f32_16x16x32_f16 v[38:41], v[64:67], v[60:63], v[40:43]
	v_mfma_f32_16x16x32_f16 v[48:51], v[68:71], v[60:63], v[48:51]
	v_mfma_f32_16x16x32_f16 v[28:31], v[72:75], v[60:63], v[30:33]
	v_mfma_f32_16x16x32_f16 v[20:23], v[76:79], v[60:63], v[20:23]
	ds_read_b128 v[56:59], v10
	ds_read_b128 v[60:63], v10 offset:2048
	ds_read_b128 v[64:67], v9 offset:16384
	ds_read_b128 v[68:71], v9 offset:18432
	ds_read_b128 v[72:75], v9 offset:20480
	ds_read_b128 v[76:79], v9 offset:22528
	s_waitcnt lgkmcnt(6)
	v_mfma_f32_16x16x32_f16 v[24:27], v[88:91], v[80:83], v[24:27]
	v_mfma_f32_16x16x32_f16 v[32:35], v[92:95], v[80:83], v[34:37]
	v_mfma_f32_16x16x32_f16 v[42:45], v[96:99], v[80:83], v[44:47]
	v_mfma_f32_16x16x32_f16 v[52:55], v[100:103], v[80:83], v[52:55]
	v_mfma_f32_16x16x32_f16 v[36:39], v[88:91], v[84:87], v[38:41]
	v_mfma_f32_16x16x32_f16 v[46:49], v[92:95], v[84:87], v[48:51]
	v_mfma_f32_16x16x32_f16 v[28:31], v[96:99], v[84:87], v[28:31]
	v_mfma_f32_16x16x32_f16 v[20:23], v[100:103], v[84:87], v[20:23]
	s_mov_b64 s[20:21], 0x300
	s_mov_b32 m0, s6
	s_waitcnt vmcnt(4) lgkmcnt(0)
	s_barrier
	v_mfma_f32_16x16x32_f16 v[24:27], v[64:67], v[56:59], v[24:27]
	v_lshl_add_u64 v[40:41], v[4:5], 0, s[20:21]
	v_lshl_add_u64 v[50:51], v[6:7], 0, s[20:21]
	s_mov_b64 s[20:21], 0x20300
	global_load_lds_dwordx4 v[50:51], off
	v_mfma_f32_16x16x32_f16 v[32:35], v[68:71], v[56:59], v[32:35]
	v_lshl_add_u64 v[50:51], v[6:7], 0, s[20:21]
	s_mov_b32 m0, s3
	s_nop 0
	global_load_lds_dwordx4 v[50:51], off
	s_mov_b32 m0, s4
	s_nop 0
	global_load_lds_dwordx4 v[40:41], off
	v_lshl_add_u64 v[40:41], v[4:5], 0, s[20:21]
	s_mov_b32 m0, s5
	s_nop 0
	global_load_lds_dwordx4 v[40:41], off
	v_mfma_f32_16x16x32_f16 v[40:43], v[72:75], v[56:59], v[42:45]
	v_mfma_f32_16x16x32_f16 v[50:53], v[76:79], v[56:59], v[52:55]
	ds_read_b128 v[80:83], v11 offset:32768
	ds_read_b128 v[84:87], v11 offset:34816
	ds_read_b128 v[88:91], v2 offset:49152
	ds_read_b128 v[92:95], v2 offset:51200
	ds_read_b128 v[96:99], v2 offset:53248
	ds_read_b128 v[100:103], v2 offset:55296
	v_mfma_f32_16x16x32_f16 v[36:39], v[64:67], v[60:63], v[36:39]
	v_mfma_f32_16x16x32_f16 v[44:47], v[68:71], v[60:63], v[46:49]
	v_mfma_f32_16x16x32_f16 v[28:31], v[72:75], v[60:63], v[28:31]
	v_mfma_f32_16x16x32_f16 v[20:23], v[76:79], v[60:63], v[20:23]
	s_waitcnt lgkmcnt(0)
	v_mfma_f32_16x16x32_f16 v[48:51], v[100:103], v[80:83], v[50:53]
	s_nop 2
	ds_read_b128 v[52:55], v10 offset:32768
	ds_read_b128 v[56:59], v10 offset:34816
	ds_read_b128 v[60:63], v9 offset:49152
	ds_read_b128 v[64:67], v9 offset:51200
	ds_read_b128 v[68:71], v9 offset:53248
	ds_read_b128 v[72:75], v9 offset:55296
	v_mfma_f32_16x16x32_f16 v[24:27], v[88:91], v[80:83], v[24:27]
	v_mfma_f32_16x16x32_f16 v[32:35], v[92:95], v[80:83], v[32:35]
	v_mfma_f32_16x16x32_f16 v[40:43], v[96:99], v[80:83], v[40:43]
	v_mfma_f32_16x16x32_f16 v[36:39], v[88:91], v[84:87], v[36:39]
	v_mfma_f32_16x16x32_f16 v[44:47], v[92:95], v[84:87], v[44:47]
	v_mfma_f32_16x16x32_f16 v[28:31], v[96:99], v[84:87], v[28:31]
	v_mfma_f32_16x16x32_f16 v[20:23], v[100:103], v[84:87], v[20:23]
	s_mov_b64 s[20:21], 0x380
	s_mov_b32 m0, s16
	s_waitcnt vmcnt(4) lgkmcnt(0)
	s_barrier
	v_mfma_f32_16x16x32_f16 v[24:27], v[60:63], v[52:55], v[24:27]
	v_lshl_add_u64 v[76:77], v[4:5], 0, s[20:21]
	v_lshl_add_u64 v[78:79], v[6:7], 0, s[20:21]
	s_mov_b64 s[20:21], 0x20380
	global_load_lds_dwordx4 v[78:79], off
	v_mfma_f32_16x16x32_f16 v[32:35], v[64:67], v[52:55], v[32:35]
	v_lshl_add_u64 v[78:79], v[6:7], 0, s[20:21]
	s_mov_b32 m0, s13
	s_nop 0
	global_load_lds_dwordx4 v[78:79], off
	v_mfma_f32_16x16x32_f16 v[40:43], v[68:71], v[52:55], v[40:43]
	s_mov_b32 m0, s14
	s_nop 0
	global_load_lds_dwordx4 v[76:77], off
	v_mfma_f32_16x16x32_f16 v[48:51], v[72:75], v[52:55], v[48:51]
	v_lshl_add_u64 v[76:77], v[4:5], 0, s[20:21]
	s_mov_b32 m0, s15
	s_nop 0
	global_load_lds_dwordx4 v[76:77], off
	ds_read_b128 v[76:79], v12
	ds_read_b128 v[80:83], v13
	ds_read_b128 v[84:87], v14
	ds_read_b128 v[88:91], v15
	ds_read_b128 v[92:95], v16
	ds_read_b128 v[96:99], v17
	v_mfma_f32_16x16x32_f16 v[36:39], v[60:63], v[56:59], v[36:39]
	v_mfma_f32_16x16x32_f16 v[44:47], v[64:67], v[56:59], v[44:47]
	v_mfma_f32_16x16x32_f16 v[28:31], v[68:71], v[56:59], v[28:31]
	v_mfma_f32_16x16x32_f16 v[20:23], v[72:75], v[56:59], v[20:23]
	ds_read_b128 v[52:55], v19
	ds_read_b128 v[56:59], v19 offset:2048
	ds_read_b128 v[60:63], v18 offset:16384
	ds_read_b128 v[64:67], v18 offset:18432
	ds_read_b128 v[68:71], v18 offset:20480
	ds_read_b128 v[72:75], v18 offset:22528
	s_waitcnt lgkmcnt(6)
	v_mfma_f32_16x16x32_f16 v[24:27], v[84:87], v[76:79], v[24:27]
	v_mfma_f32_16x16x32_f16 v[32:35], v[88:91], v[76:79], v[32:35]
	v_mfma_f32_16x16x32_f16 v[40:43], v[92:95], v[76:79], v[40:43]
	v_mfma_f32_16x16x32_f16 v[48:51], v[96:99], v[76:79], v[48:51]
	v_mfma_f32_16x16x32_f16 v[36:39], v[84:87], v[80:83], v[36:39]
	v_mfma_f32_16x16x32_f16 v[44:47], v[88:91], v[80:83], v[44:47]
	v_mfma_f32_16x16x32_f16 v[28:31], v[92:95], v[80:83], v[28:31]
	v_mfma_f32_16x16x32_f16 v[20:23], v[96:99], v[80:83], v[20:23]
	s_mov_b64 s[20:21], 0x400
	s_mov_b32 m0, s18
	s_waitcnt vmcnt(4) lgkmcnt(0)
	s_barrier
	v_mfma_f32_16x16x32_f16 v[24:27], v[60:63], v[52:55], v[24:27]
	v_lshl_add_u64 v[76:77], v[4:5], 0, s[20:21]
	v_lshl_add_u64 v[78:79], v[6:7], 0, s[20:21]
	s_mov_b64 s[20:21], 0x20400
	global_load_lds_dwordx4 v[78:79], off
	v_mfma_f32_16x16x32_f16 v[32:35], v[64:67], v[52:55], v[32:35]
	v_lshl_add_u64 v[78:79], v[6:7], 0, s[20:21]
	s_mov_b32 m0, s17
	s_nop 0
	global_load_lds_dwordx4 v[78:79], off
	v_mfma_f32_16x16x32_f16 v[40:43], v[68:71], v[52:55], v[40:43]
	s_mov_b32 m0, s7
	s_nop 0
	global_load_lds_dwordx4 v[76:77], off
	v_mfma_f32_16x16x32_f16 v[48:51], v[72:75], v[52:55], v[48:51]
	v_lshl_add_u64 v[76:77], v[4:5], 0, s[20:21]
	s_mov_b32 m0, s12
	s_nop 0
	global_load_lds_dwordx4 v[76:77], off
	ds_read_b128 v[76:79], v11
	ds_read_b128 v[80:83], v11 offset:2048
	ds_read_b128 v[84:87], v2 offset:16384
	ds_read_b128 v[88:91], v2 offset:18432
	ds_read_b128 v[92:95], v2 offset:20480
	ds_read_b128 v[96:99], v2 offset:22528
	v_mfma_f32_16x16x32_f16 v[36:39], v[60:63], v[56:59], v[36:39]
	v_mfma_f32_16x16x32_f16 v[44:47], v[64:67], v[56:59], v[44:47]
	v_mfma_f32_16x16x32_f16 v[28:31], v[68:71], v[56:59], v[28:31]
	v_mfma_f32_16x16x32_f16 v[20:23], v[72:75], v[56:59], v[20:23]
	ds_read_b128 v[52:55], v10
	ds_read_b128 v[56:59], v10 offset:2048
	ds_read_b128 v[60:63], v9 offset:16384
	ds_read_b128 v[64:67], v9 offset:18432
	ds_read_b128 v[68:71], v9 offset:20480
	ds_read_b128 v[72:75], v9 offset:22528
	s_waitcnt lgkmcnt(6)
	v_mfma_f32_16x16x32_f16 v[24:27], v[84:87], v[76:79], v[24:27]
	v_mfma_f32_16x16x32_f16 v[32:35], v[88:91], v[76:79], v[32:35]
	v_mfma_f32_16x16x32_f16 v[40:43], v[92:95], v[76:79], v[40:43]
	v_mfma_f32_16x16x32_f16 v[48:51], v[96:99], v[76:79], v[48:51]
	v_mfma_f32_16x16x32_f16 v[36:39], v[84:87], v[80:83], v[36:39]
	v_mfma_f32_16x16x32_f16 v[44:47], v[88:91], v[80:83], v[44:47]
	v_mfma_f32_16x16x32_f16 v[28:31], v[92:95], v[80:83], v[28:31]
	v_mfma_f32_16x16x32_f16 v[20:23], v[96:99], v[80:83], v[20:23]
	s_mov_b64 s[20:21], 0x480
	s_mov_b32 m0, s6
	s_waitcnt vmcnt(4) lgkmcnt(0)
	s_barrier
	v_mfma_f32_16x16x32_f16 v[24:27], v[60:63], v[52:55], v[24:27]
	v_lshl_add_u64 v[76:77], v[4:5], 0, s[20:21]
	v_lshl_add_u64 v[78:79], v[6:7], 0, s[20:21]
	s_mov_b64 s[20:21], 0x20480
	global_load_lds_dwordx4 v[78:79], off
	v_mfma_f32_16x16x32_f16 v[32:35], v[64:67], v[52:55], v[32:35]
	v_lshl_add_u64 v[78:79], v[6:7], 0, s[20:21]
	s_mov_b32 m0, s3
	s_nop 0
	global_load_lds_dwordx4 v[78:79], off
	v_mfma_f32_16x16x32_f16 v[40:43], v[68:71], v[52:55], v[40:43]
	s_mov_b32 m0, s4
	s_nop 0
	global_load_lds_dwordx4 v[76:77], off
	v_mfma_f32_16x16x32_f16 v[48:51], v[72:75], v[52:55], v[48:51]
	v_lshl_add_u64 v[76:77], v[4:5], 0, s[20:21]
	s_mov_b32 m0, s5
	s_nop 0
	global_load_lds_dwordx4 v[76:77], off
	ds_read_b128 v[76:79], v11 offset:32768
	ds_read_b128 v[80:83], v11 offset:34816
	ds_read_b128 v[84:87], v2 offset:49152
	ds_read_b128 v[88:91], v2 offset:51200
	ds_read_b128 v[92:95], v2 offset:53248
	ds_read_b128 v[96:99], v2 offset:55296
	v_mfma_f32_16x16x32_f16 v[36:39], v[60:63], v[56:59], v[36:39]
	v_mfma_f32_16x16x32_f16 v[44:47], v[64:67], v[56:59], v[44:47]
	v_mfma_f32_16x16x32_f16 v[28:31], v[68:71], v[56:59], v[28:31]
	v_mfma_f32_16x16x32_f16 v[20:23], v[72:75], v[56:59], v[20:23]
	ds_read_b128 v[52:55], v10 offset:32768
	ds_read_b128 v[56:59], v10 offset:34816
	ds_read_b128 v[60:63], v9 offset:49152
	ds_read_b128 v[64:67], v9 offset:51200
	ds_read_b128 v[68:71], v9 offset:53248
	ds_read_b128 v[72:75], v9 offset:55296
	s_waitcnt lgkmcnt(6)
	v_mfma_f32_16x16x32_f16 v[24:27], v[84:87], v[76:79], v[24:27]
	v_mfma_f32_16x16x32_f16 v[32:35], v[88:91], v[76:79], v[32:35]
	v_mfma_f32_16x16x32_f16 v[40:43], v[92:95], v[76:79], v[40:43]
	v_mfma_f32_16x16x32_f16 v[48:51], v[96:99], v[76:79], v[48:51]
	v_mfma_f32_16x16x32_f16 v[36:39], v[84:87], v[80:83], v[36:39]
	v_mfma_f32_16x16x32_f16 v[44:47], v[88:91], v[80:83], v[44:47]
	v_mfma_f32_16x16x32_f16 v[28:31], v[92:95], v[80:83], v[28:31]
	v_mfma_f32_16x16x32_f16 v[20:23], v[96:99], v[80:83], v[20:23]
	s_mov_b64 s[20:21], 0x500
	s_mov_b32 m0, s16
	s_waitcnt vmcnt(4) lgkmcnt(0)
	s_barrier
	v_mfma_f32_16x16x32_f16 v[24:27], v[60:63], v[52:55], v[24:27]
	v_lshl_add_u64 v[76:77], v[4:5], 0, s[20:21]
	v_lshl_add_u64 v[78:79], v[6:7], 0, s[20:21]
	s_mov_b64 s[20:21], 0x20500
	global_load_lds_dwordx4 v[78:79], off
	v_mfma_f32_16x16x32_f16 v[32:35], v[64:67], v[52:55], v[32:35]
	v_lshl_add_u64 v[78:79], v[6:7], 0, s[20:21]
	s_mov_b32 m0, s13
	s_nop 0
	global_load_lds_dwordx4 v[78:79], off
	v_mfma_f32_16x16x32_f16 v[40:43], v[68:71], v[52:55], v[40:43]
	s_mov_b32 m0, s14
	s_nop 0
	global_load_lds_dwordx4 v[76:77], off
	v_mfma_f32_16x16x32_f16 v[48:51], v[72:75], v[52:55], v[48:51]
	v_lshl_add_u64 v[76:77], v[4:5], 0, s[20:21]
	s_mov_b32 m0, s15
	s_nop 0
	global_load_lds_dwordx4 v[76:77], off
	ds_read_b128 v[76:79], v12
	ds_read_b128 v[80:83], v13
	ds_read_b128 v[84:87], v14
	ds_read_b128 v[88:91], v15
	ds_read_b128 v[92:95], v16
	ds_read_b128 v[96:99], v17
	v_mfma_f32_16x16x32_f16 v[36:39], v[60:63], v[56:59], v[36:39]
	v_mfma_f32_16x16x32_f16 v[44:47], v[64:67], v[56:59], v[44:47]
	v_mfma_f32_16x16x32_f16 v[28:31], v[68:71], v[56:59], v[28:31]
	v_mfma_f32_16x16x32_f16 v[20:23], v[72:75], v[56:59], v[20:23]
	ds_read_b128 v[52:55], v19
	ds_read_b128 v[56:59], v19 offset:2048
	ds_read_b128 v[60:63], v18 offset:16384
	ds_read_b128 v[64:67], v18 offset:18432
	ds_read_b128 v[68:71], v18 offset:20480
	ds_read_b128 v[72:75], v18 offset:22528
	s_waitcnt lgkmcnt(6)
	v_mfma_f32_16x16x32_f16 v[24:27], v[84:87], v[76:79], v[24:27]
	v_mfma_f32_16x16x32_f16 v[32:35], v[88:91], v[76:79], v[32:35]
	v_mfma_f32_16x16x32_f16 v[40:43], v[92:95], v[76:79], v[40:43]
	v_mfma_f32_16x16x32_f16 v[48:51], v[96:99], v[76:79], v[48:51]
	v_mfma_f32_16x16x32_f16 v[36:39], v[84:87], v[80:83], v[36:39]
	v_mfma_f32_16x16x32_f16 v[44:47], v[88:91], v[80:83], v[44:47]
	v_mfma_f32_16x16x32_f16 v[28:31], v[92:95], v[80:83], v[28:31]
	v_mfma_f32_16x16x32_f16 v[20:23], v[96:99], v[80:83], v[20:23]
	s_mov_b64 s[20:21], 0x580
	s_mov_b32 m0, s18
	s_waitcnt vmcnt(4) lgkmcnt(0)
	s_barrier
	v_mfma_f32_16x16x32_f16 v[24:27], v[60:63], v[52:55], v[24:27]
	v_lshl_add_u64 v[76:77], v[4:5], 0, s[20:21]
	v_lshl_add_u64 v[78:79], v[6:7], 0, s[20:21]
	s_mov_b64 s[20:21], 0x20580
	global_load_lds_dwordx4 v[78:79], off
	v_mfma_f32_16x16x32_f16 v[32:35], v[64:67], v[52:55], v[32:35]
	v_lshl_add_u64 v[78:79], v[6:7], 0, s[20:21]
	s_mov_b32 m0, s17
	s_nop 0
	global_load_lds_dwordx4 v[78:79], off
	v_mfma_f32_16x16x32_f16 v[40:43], v[68:71], v[52:55], v[40:43]
	s_mov_b32 m0, s7
	s_nop 0
	global_load_lds_dwordx4 v[76:77], off
	v_mfma_f32_16x16x32_f16 v[48:51], v[72:75], v[52:55], v[48:51]
	v_lshl_add_u64 v[76:77], v[4:5], 0, s[20:21]
	s_mov_b32 m0, s12
	s_nop 0
	global_load_lds_dwordx4 v[76:77], off
	ds_read_b128 v[76:79], v11
	ds_read_b128 v[80:83], v11 offset:2048
	ds_read_b128 v[84:87], v2 offset:16384
	ds_read_b128 v[88:91], v2 offset:18432
	ds_read_b128 v[92:95], v2 offset:20480
	ds_read_b128 v[96:99], v2 offset:22528
	v_mfma_f32_16x16x32_f16 v[36:39], v[60:63], v[56:59], v[36:39]
	v_mfma_f32_16x16x32_f16 v[44:47], v[64:67], v[56:59], v[44:47]
	v_mfma_f32_16x16x32_f16 v[28:31], v[68:71], v[56:59], v[28:31]
	v_mfma_f32_16x16x32_f16 v[20:23], v[72:75], v[56:59], v[20:23]
	ds_read_b128 v[52:55], v10
	ds_read_b128 v[56:59], v10 offset:2048
	ds_read_b128 v[60:63], v9 offset:16384
	ds_read_b128 v[64:67], v9 offset:18432
	ds_read_b128 v[68:71], v9 offset:20480
	ds_read_b128 v[72:75], v9 offset:22528
	s_waitcnt lgkmcnt(6)
	v_mfma_f32_16x16x32_f16 v[24:27], v[84:87], v[76:79], v[24:27]
	v_mfma_f32_16x16x32_f16 v[32:35], v[88:91], v[76:79], v[32:35]
	v_mfma_f32_16x16x32_f16 v[40:43], v[92:95], v[76:79], v[40:43]
	v_mfma_f32_16x16x32_f16 v[48:51], v[96:99], v[76:79], v[48:51]
	v_mfma_f32_16x16x32_f16 v[36:39], v[84:87], v[80:83], v[36:39]
	v_mfma_f32_16x16x32_f16 v[44:47], v[88:91], v[80:83], v[44:47]
	v_mfma_f32_16x16x32_f16 v[28:31], v[92:95], v[80:83], v[28:31]
	v_mfma_f32_16x16x32_f16 v[20:23], v[96:99], v[80:83], v[20:23]
	s_mov_b64 s[20:21], 0x600
	s_mov_b32 m0, s6
	s_waitcnt vmcnt(4) lgkmcnt(0)
	s_barrier
	v_mfma_f32_16x16x32_f16 v[24:27], v[60:63], v[52:55], v[24:27]
	v_lshl_add_u64 v[76:77], v[4:5], 0, s[20:21]
	v_lshl_add_u64 v[78:79], v[6:7], 0, s[20:21]
	s_mov_b64 s[20:21], 0x20600
	global_load_lds_dwordx4 v[78:79], off
	v_mfma_f32_16x16x32_f16 v[32:35], v[64:67], v[52:55], v[32:35]
	v_lshl_add_u64 v[78:79], v[6:7], 0, s[20:21]
	s_mov_b32 m0, s3
	s_nop 0
	global_load_lds_dwordx4 v[78:79], off
	v_mfma_f32_16x16x32_f16 v[40:43], v[68:71], v[52:55], v[40:43]
	s_mov_b32 m0, s4
	s_nop 0
	global_load_lds_dwordx4 v[76:77], off
	v_mfma_f32_16x16x32_f16 v[48:51], v[72:75], v[52:55], v[48:51]
	v_lshl_add_u64 v[76:77], v[4:5], 0, s[20:21]
	s_mov_b32 m0, s5
	s_nop 0
	global_load_lds_dwordx4 v[76:77], off
	ds_read_b128 v[76:79], v11 offset:32768
	ds_read_b128 v[80:83], v11 offset:34816
	ds_read_b128 v[84:87], v2 offset:49152
	ds_read_b128 v[88:91], v2 offset:51200
	ds_read_b128 v[92:95], v2 offset:53248
	ds_read_b128 v[96:99], v2 offset:55296
	v_mfma_f32_16x16x32_f16 v[36:39], v[60:63], v[56:59], v[36:39]
	v_mfma_f32_16x16x32_f16 v[44:47], v[64:67], v[56:59], v[44:47]
	v_mfma_f32_16x16x32_f16 v[28:31], v[68:71], v[56:59], v[28:31]
	v_mfma_f32_16x16x32_f16 v[20:23], v[72:75], v[56:59], v[20:23]
	ds_read_b128 v[52:55], v10 offset:32768
	ds_read_b128 v[56:59], v10 offset:34816
	ds_read_b128 v[60:63], v9 offset:49152
	ds_read_b128 v[64:67], v9 offset:51200
	ds_read_b128 v[68:71], v9 offset:53248
	ds_read_b128 v[72:75], v9 offset:55296
	s_waitcnt lgkmcnt(6)
	v_mfma_f32_16x16x32_f16 v[24:27], v[84:87], v[76:79], v[24:27]
	v_mfma_f32_16x16x32_f16 v[32:35], v[88:91], v[76:79], v[32:35]
	v_mfma_f32_16x16x32_f16 v[40:43], v[92:95], v[76:79], v[40:43]
	v_mfma_f32_16x16x32_f16 v[48:51], v[96:99], v[76:79], v[48:51]
	v_mfma_f32_16x16x32_f16 v[36:39], v[84:87], v[80:83], v[36:39]
	v_mfma_f32_16x16x32_f16 v[44:47], v[88:91], v[80:83], v[44:47]
	v_mfma_f32_16x16x32_f16 v[28:31], v[92:95], v[80:83], v[28:31]
	v_mfma_f32_16x16x32_f16 v[20:23], v[96:99], v[80:83], v[20:23]
	s_mov_b64 s[20:21], 0x680
	s_mov_b32 m0, s16
	s_waitcnt vmcnt(4) lgkmcnt(0)
	s_barrier
	v_mfma_f32_16x16x32_f16 v[24:27], v[60:63], v[52:55], v[24:27]
	v_lshl_add_u64 v[76:77], v[4:5], 0, s[20:21]
	v_lshl_add_u64 v[78:79], v[6:7], 0, s[20:21]
	s_mov_b64 s[20:21], 0x20680
	global_load_lds_dwordx4 v[78:79], off
	v_mfma_f32_16x16x32_f16 v[32:35], v[64:67], v[52:55], v[32:35]
	v_lshl_add_u64 v[78:79], v[6:7], 0, s[20:21]
	s_mov_b32 m0, s13
	s_nop 0
	global_load_lds_dwordx4 v[78:79], off
	v_mfma_f32_16x16x32_f16 v[40:43], v[68:71], v[52:55], v[40:43]
	s_mov_b32 m0, s14
	s_nop 0
	global_load_lds_dwordx4 v[76:77], off
	v_mfma_f32_16x16x32_f16 v[48:51], v[72:75], v[52:55], v[48:51]
	v_lshl_add_u64 v[76:77], v[4:5], 0, s[20:21]
	s_mov_b32 m0, s15
	s_nop 0
	global_load_lds_dwordx4 v[76:77], off
	ds_read_b128 v[76:79], v12
	ds_read_b128 v[80:83], v13
	ds_read_b128 v[84:87], v14
	ds_read_b128 v[88:91], v15
	ds_read_b128 v[92:95], v16
	ds_read_b128 v[96:99], v17
	v_mfma_f32_16x16x32_f16 v[36:39], v[60:63], v[56:59], v[36:39]
	v_mfma_f32_16x16x32_f16 v[44:47], v[64:67], v[56:59], v[44:47]
	v_mfma_f32_16x16x32_f16 v[28:31], v[68:71], v[56:59], v[28:31]
	v_mfma_f32_16x16x32_f16 v[20:23], v[72:75], v[56:59], v[20:23]
	ds_read_b128 v[52:55], v19
	ds_read_b128 v[56:59], v19 offset:2048
	ds_read_b128 v[60:63], v18 offset:16384
	ds_read_b128 v[64:67], v18 offset:18432
	ds_read_b128 v[68:71], v18 offset:20480
	ds_read_b128 v[72:75], v18 offset:22528
	s_waitcnt lgkmcnt(6)
	v_mfma_f32_16x16x32_f16 v[24:27], v[84:87], v[76:79], v[24:27]
	v_mfma_f32_16x16x32_f16 v[32:35], v[88:91], v[76:79], v[32:35]
	v_mfma_f32_16x16x32_f16 v[40:43], v[92:95], v[76:79], v[40:43]
	v_mfma_f32_16x16x32_f16 v[48:51], v[96:99], v[76:79], v[48:51]
	v_mfma_f32_16x16x32_f16 v[36:39], v[84:87], v[80:83], v[36:39]
	v_mfma_f32_16x16x32_f16 v[44:47], v[88:91], v[80:83], v[44:47]
	v_mfma_f32_16x16x32_f16 v[28:31], v[92:95], v[80:83], v[28:31]
	v_mfma_f32_16x16x32_f16 v[20:23], v[96:99], v[80:83], v[20:23]
	s_mov_b64 s[14:15], 0x700
	s_mov_b32 m0, s18
	s_waitcnt vmcnt(4) lgkmcnt(0)
	s_barrier
	v_mfma_f32_16x16x32_f16 v[24:27], v[60:63], v[52:55], v[24:27]
	v_lshl_add_u64 v[76:77], v[4:5], 0, s[14:15]
	v_lshl_add_u64 v[78:79], v[6:7], 0, s[14:15]
	s_mov_b64 s[14:15], 0x20700
	global_load_lds_dwordx4 v[78:79], off
	v_mfma_f32_16x16x32_f16 v[32:35], v[64:67], v[52:55], v[32:35]
	v_lshl_add_u64 v[78:79], v[6:7], 0, s[14:15]
	s_mov_b32 m0, s17
	s_nop 0
	global_load_lds_dwordx4 v[78:79], off
	v_mfma_f32_16x16x32_f16 v[40:43], v[68:71], v[52:55], v[40:43]
	s_mov_b32 m0, s7
	s_nop 0
	global_load_lds_dwordx4 v[76:77], off
	v_mfma_f32_16x16x32_f16 v[48:51], v[72:75], v[52:55], v[48:51]
	v_lshl_add_u64 v[76:77], v[4:5], 0, s[14:15]
	s_mov_b32 m0, s12
	s_nop 0
	global_load_lds_dwordx4 v[76:77], off
	ds_read_b128 v[76:79], v11
	ds_read_b128 v[80:83], v11 offset:2048
	ds_read_b128 v[84:87], v2 offset:16384
	ds_read_b128 v[88:91], v2 offset:18432
	ds_read_b128 v[92:95], v2 offset:20480
	ds_read_b128 v[96:99], v2 offset:22528
	v_mfma_f32_16x16x32_f16 v[36:39], v[60:63], v[56:59], v[36:39]
	v_mfma_f32_16x16x32_f16 v[44:47], v[64:67], v[56:59], v[44:47]
	v_mfma_f32_16x16x32_f16 v[28:31], v[68:71], v[56:59], v[28:31]
	v_mfma_f32_16x16x32_f16 v[20:23], v[72:75], v[56:59], v[20:23]
	ds_read_b128 v[52:55], v10
	ds_read_b128 v[56:59], v10 offset:2048
	ds_read_b128 v[60:63], v9 offset:16384
	ds_read_b128 v[64:67], v9 offset:18432
	ds_read_b128 v[68:71], v9 offset:20480
	ds_read_b128 v[72:75], v9 offset:22528
	s_waitcnt lgkmcnt(6)
	v_mfma_f32_16x16x32_f16 v[24:27], v[84:87], v[76:79], v[24:27]
	v_mfma_f32_16x16x32_f16 v[32:35], v[88:91], v[76:79], v[32:35]
	v_mfma_f32_16x16x32_f16 v[40:43], v[92:95], v[76:79], v[40:43]
	v_mfma_f32_16x16x32_f16 v[48:51], v[96:99], v[76:79], v[48:51]
	v_mfma_f32_16x16x32_f16 v[36:39], v[84:87], v[80:83], v[36:39]
	v_mfma_f32_16x16x32_f16 v[44:47], v[88:91], v[80:83], v[44:47]
	v_mfma_f32_16x16x32_f16 v[28:31], v[92:95], v[80:83], v[28:31]
	v_mfma_f32_16x16x32_f16 v[20:23], v[96:99], v[80:83], v[20:23]
	s_mov_b32 m0, s6
	s_mov_b64 s[6:7], 0x780
	s_waitcnt vmcnt(4) lgkmcnt(0)
	s_barrier
	v_mfma_f32_16x16x32_f16 v[24:27], v[60:63], v[52:55], v[24:27]
	v_lshl_add_u64 v[76:77], v[4:5], 0, s[6:7]
	v_lshl_add_u64 v[78:79], v[6:7], 0, s[6:7]
	s_mov_b64 s[6:7], 0x20780
	global_load_lds_dwordx4 v[78:79], off
	v_mfma_f32_16x16x32_f16 v[32:35], v[64:67], v[52:55], v[32:35]
	v_lshl_add_u64 v[6:7], v[6:7], 0, s[6:7]
	s_mov_b32 m0, s3
	v_lshl_add_u64 v[4:5], v[4:5], 0, s[6:7]
	global_load_lds_dwordx4 v[6:7], off
	v_mfma_f32_16x16x32_f16 v[40:43], v[68:71], v[52:55], v[40:43]
	s_mov_b32 m0, s4
	s_nop 0
	global_load_lds_dwordx4 v[76:77], off
	v_mfma_f32_16x16x32_f16 v[48:51], v[72:75], v[52:55], v[48:51]
	s_mov_b32 m0, s5
	s_nop 0
	global_load_lds_dwordx4 v[4:5], off
	ds_read_b128 v[4:7], v11 offset:32768
	ds_read_b128 v[76:79], v11 offset:34816
	ds_read_b128 v[80:83], v2 offset:49152
	ds_read_b128 v[84:87], v2 offset:51200
	ds_read_b128 v[88:91], v2 offset:53248
	ds_read_b128 v[92:95], v2 offset:55296
	v_mfma_f32_16x16x32_f16 v[36:39], v[60:63], v[56:59], v[36:39]
	v_mfma_f32_16x16x32_f16 v[44:47], v[64:67], v[56:59], v[44:47]
	v_mfma_f32_16x16x32_f16 v[28:31], v[68:71], v[56:59], v[28:31]
	v_mfma_f32_16x16x32_f16 v[20:23], v[72:75], v[56:59], v[20:23]
	s_waitcnt lgkmcnt(0)
	v_mfma_f32_16x16x32_f16 v[24:27], v[80:83], v[4:7], v[24:27]
	v_mfma_f32_16x16x32_f16 v[32:35], v[84:87], v[4:7], v[32:35]
	v_mfma_f32_16x16x32_f16 v[40:43], v[88:91], v[4:7], v[40:43]
	v_mfma_f32_16x16x32_f16 v[4:7], v[92:95], v[4:7], v[48:51]
	s_nop 2
	ds_read_b128 v[48:51], v10 offset:32768
	ds_read_b128 v[52:55], v10 offset:34816
	ds_read_b128 v[56:59], v9 offset:49152
	ds_read_b128 v[60:63], v9 offset:51200
	ds_read_b128 v[64:67], v9 offset:53248
	ds_read_b128 v[68:71], v9 offset:55296
	v_mfma_f32_16x16x32_f16 v[36:39], v[80:83], v[76:79], v[36:39]
	v_mfma_f32_16x16x32_f16 v[44:47], v[84:87], v[76:79], v[44:47]
	v_mfma_f32_16x16x32_f16 v[28:31], v[88:91], v[76:79], v[28:31]
	v_mfma_f32_16x16x32_f16 v[20:23], v[92:95], v[76:79], v[20:23]
	s_waitcnt vmcnt(4) lgkmcnt(0)
	s_barrier
	ds_read_b128 v[72:75], v12
	ds_read_b128 v[76:79], v13
	ds_read_b128 v[80:83], v14
	ds_read_b128 v[12:15], v15
	ds_read_b128 v[84:87], v16
	ds_read_b128 v[88:91], v17
	v_mfma_f32_16x16x32_f16 v[24:27], v[56:59], v[48:51], v[24:27]
	v_mfma_f32_16x16x32_f16 v[32:35], v[60:63], v[48:51], v[32:35]
	v_mfma_f32_16x16x32_f16 v[40:43], v[64:67], v[48:51], v[40:43]
	v_mfma_f32_16x16x32_f16 v[4:7], v[68:71], v[48:51], v[4:7]
	v_mfma_f32_16x16x32_f16 v[36:39], v[56:59], v[52:55], v[36:39]
	v_mfma_f32_16x16x32_f16 v[44:47], v[60:63], v[52:55], v[44:47]
	v_mfma_f32_16x16x32_f16 v[28:31], v[64:67], v[52:55], v[28:31]
	v_mfma_f32_16x16x32_f16 v[20:23], v[68:71], v[52:55], v[20:23]
	s_waitcnt lgkmcnt(0)
	v_mfma_f32_16x16x32_f16 v[32:35], v[12:15], v[72:75], v[32:35]
	v_mfma_f32_16x16x32_f16 v[12:15], v[12:15], v[76:79], v[44:47]
	s_nop 2
	ds_read_b128 v[44:47], v19
	ds_read_b128 v[48:51], v19 offset:2048
	ds_read_b128 v[52:55], v18 offset:16384
	ds_read_b128 v[56:59], v18 offset:18432
	ds_read_b128 v[60:63], v18 offset:20480
	ds_read_b128 v[16:19], v18 offset:22528
	v_mfma_f32_16x16x32_f16 v[24:27], v[80:83], v[72:75], v[24:27]
	v_mfma_f32_16x16x32_f16 v[40:43], v[84:87], v[72:75], v[40:43]
	v_mfma_f32_16x16x32_f16 v[4:7], v[88:91], v[72:75], v[4:7]
	v_mfma_f32_16x16x32_f16 v[36:39], v[80:83], v[76:79], v[36:39]
	v_mfma_f32_16x16x32_f16 v[28:31], v[84:87], v[76:79], v[28:31]
	v_mfma_f32_16x16x32_f16 v[20:23], v[88:91], v[76:79], v[20:23]
	s_waitcnt vmcnt(0) lgkmcnt(0)
	s_barrier
	ds_read_b128 v[64:67], v11
	ds_read_b128 v[68:71], v11 offset:2048
	ds_read_b128 v[72:75], v2 offset:16384
	ds_read_b128 v[76:79], v2 offset:18432
	ds_read_b128 v[80:83], v2 offset:20480
	ds_read_b128 v[84:87], v2 offset:22528
	v_mfma_f32_16x16x32_f16 v[24:27], v[52:55], v[44:47], v[24:27]
	v_mfma_f32_16x16x32_f16 v[32:35], v[56:59], v[44:47], v[32:35]
	v_mfma_f32_16x16x32_f16 v[40:43], v[60:63], v[44:47], v[40:43]
	v_mfma_f32_16x16x32_f16 v[4:7], v[16:19], v[44:47], v[4:7]
	v_mfma_f32_16x16x32_f16 v[36:39], v[52:55], v[48:51], v[36:39]
	v_mfma_f32_16x16x32_f16 v[12:15], v[56:59], v[48:51], v[12:15]
	v_mfma_f32_16x16x32_f16 v[28:31], v[60:63], v[48:51], v[28:31]
	v_mfma_f32_16x16x32_f16 v[16:19], v[16:19], v[48:51], v[20:23]
	s_waitcnt lgkmcnt(3)
	v_mfma_f32_16x16x32_f16 v[20:23], v[72:75], v[64:67], v[24:27]
	s_waitcnt lgkmcnt(2)
	v_mfma_f32_16x16x32_f16 v[24:27], v[76:79], v[64:67], v[32:35]
	s_waitcnt lgkmcnt(1)
	v_mfma_f32_16x16x32_f16 v[32:35], v[80:83], v[64:67], v[40:43]
	s_nop 2
	ds_read_b128 v[40:43], v10
	ds_read_b128 v[44:47], v10 offset:2048
	ds_read_b128 v[48:51], v9 offset:16384
	ds_read_b128 v[52:55], v9 offset:18432
	ds_read_b128 v[56:59], v9 offset:20480
	ds_read_b128 v[60:63], v9 offset:22528
	s_waitcnt lgkmcnt(6)
	v_mfma_f32_16x16x32_f16 v[4:7], v[84:87], v[64:67], v[4:7]
	v_mfma_f32_16x16x32_f16 v[36:39], v[72:75], v[68:71], v[36:39]
	v_mfma_f32_16x16x32_f16 v[12:15], v[76:79], v[68:71], v[12:15]
	v_mfma_f32_16x16x32_f16 v[28:31], v[80:83], v[68:71], v[28:31]
	v_mfma_f32_16x16x32_f16 v[16:19], v[84:87], v[68:71], v[16:19]
	s_waitcnt vmcnt(0) lgkmcnt(0)
	s_barrier
	v_and_b32_e32 v2, 64, v0
	v_lshrrev_b32_e32 v9, 6, v0
	v_mfma_f32_16x16x32_f16 v[20:23], v[48:51], v[40:43], v[20:23]
	v_mfma_f32_16x16x32_f16 v[24:27], v[52:55], v[40:43], v[24:27]
	v_mfma_f32_16x16x32_f16 v[32:35], v[56:59], v[40:43], v[32:35]
	v_mfma_f32_16x16x32_f16 v[4:7], v[60:63], v[40:43], v[4:7]
	v_mfma_f32_16x16x32_f16 v[36:39], v[48:51], v[44:47], v[36:39]
	v_mfma_f32_16x16x32_f16 v[10:13], v[52:55], v[44:47], v[12:15]
	v_mfma_f32_16x16x32_f16 v[28:31], v[56:59], v[44:47], v[28:31]
	v_mfma_f32_16x16x32_f16 v[14:17], v[60:63], v[44:47], v[16:19]
	s_movk_i32 s3, 0x2200
	v_mad_u32_u24 v9, v9, s3, 0
	s_nop 0
	v_and_b32_e32 v18, 48, v0
	v_mul_u32_u24_e32 v19, 0x110, v8
	v_add3_u32 v18, v9, v18, v19
	s_barrier
	ds_write_b128 v18, v[20:23]
	ds_write_b128 v18, v[24:27] offset:64
	ds_write_b128 v18, v[32:35] offset:128
	ds_write_b128 v18, v[4:7] offset:192
	ds_write_b128 v18, v[36:39] offset:4352
	ds_write_b128 v18, v[10:13] offset:4416
	ds_write_b128 v18, v[28:31] offset:4480
	ds_write_b128 v18, v[14:17] offset:4544
	v_lshlrev_b32_e32 v4, 2, v8
	v_or3_b32 v2, v4, v2, s2
	v_lshlrev_b64 v[10:11], 2, v[2:3]
	s_waitcnt lgkmcnt(0)
	v_lshl_add_u64 v[2:3], s[10:11], 0, v[10:11]
	global_load_dwordx4 v[2:5], v[2:3], off
	v_bfe_u32 v0, v0, 4, 2
	v_lshlrev_b32_e32 v6, 4, v8
	v_mul_u32_u24_e32 v7, 0x110, v0
	v_add3_u32 v13, v9, v6, v7
	ds_read_b128 v[6:9], v13
	v_or3_b32 v12, s1, v1, v0
	v_mad_i64_i32 v[0:1], s[2:3], v12, s0, 0
	v_lshl_add_u64 v[0:1], v[0:1], 2, s[8:9]
	v_lshl_add_u64 v[0:1], v[0:1], 0, v[10:11]
	v_or_b32_e32 v14, 4, v12
	v_or_b32_e32 v15, 8, v12
	v_or_b32_e32 v16, 12, v12
	v_or_b32_e32 v17, 16, v12
	v_or_b32_e32 v18, 20, v12
	v_or_b32_e32 v19, 24, v12
	v_or_b32_e32 v12, 28, v12
	s_waitcnt vmcnt(0) lgkmcnt(0)
	v_pk_add_f32 v[8:9], v[4:5], v[8:9]
	v_pk_add_f32 v[6:7], v[2:3], v[6:7]
	s_nop 0
	global_store_dwordx4 v[0:1], v[6:9], off sc1
	s_nop 1
	ds_read_b128 v[6:9], v13 offset:1088
	v_mad_i64_i32 v[0:1], s[2:3], v14, s0, 0
	v_lshl_add_u64 v[0:1], v[0:1], 2, s[8:9]
	v_lshl_add_u64 v[0:1], v[0:1], 0, v[10:11]
	s_waitcnt lgkmcnt(0)
	v_pk_add_f32 v[8:9], v[4:5], v[8:9]
	v_pk_add_f32 v[6:7], v[2:3], v[6:7]
	s_nop 0
	global_store_dwordx4 v[0:1], v[6:9], off sc1
	s_nop 1
	ds_read_b128 v[6:9], v13 offset:2176
	v_mad_i64_i32 v[0:1], s[2:3], v15, s0, 0
	v_lshl_add_u64 v[0:1], v[0:1], 2, s[8:9]
	v_lshl_add_u64 v[0:1], v[0:1], 0, v[10:11]
	s_waitcnt lgkmcnt(0)
	v_pk_add_f32 v[8:9], v[4:5], v[8:9]
	v_pk_add_f32 v[6:7], v[2:3], v[6:7]
	s_nop 0
	global_store_dwordx4 v[0:1], v[6:9], off sc1
	s_nop 1
	ds_read_b128 v[6:9], v13 offset:3264
	v_mad_i64_i32 v[0:1], s[2:3], v16, s0, 0
	v_lshl_add_u64 v[0:1], v[0:1], 2, s[8:9]
	v_lshl_add_u64 v[0:1], v[0:1], 0, v[10:11]
	s_waitcnt lgkmcnt(0)
	v_pk_add_f32 v[8:9], v[4:5], v[8:9]
	v_pk_add_f32 v[6:7], v[2:3], v[6:7]
	s_nop 0
	global_store_dwordx4 v[0:1], v[6:9], off sc1
	s_nop 1
	ds_read_b128 v[6:9], v13 offset:4352
	v_mad_i64_i32 v[0:1], s[2:3], v17, s0, 0
	v_lshl_add_u64 v[0:1], v[0:1], 2, s[8:9]
	v_lshl_add_u64 v[0:1], v[0:1], 0, v[10:11]
	s_waitcnt lgkmcnt(0)
	v_pk_add_f32 v[8:9], v[4:5], v[8:9]
	v_pk_add_f32 v[6:7], v[2:3], v[6:7]
	s_nop 0
	global_store_dwordx4 v[0:1], v[6:9], off sc1
	s_nop 1
	ds_read_b128 v[6:9], v13 offset:5440
	v_mad_i64_i32 v[0:1], s[2:3], v18, s0, 0
	v_lshl_add_u64 v[0:1], v[0:1], 2, s[8:9]
	v_lshl_add_u64 v[0:1], v[0:1], 0, v[10:11]
	s_waitcnt lgkmcnt(0)
	v_pk_add_f32 v[8:9], v[4:5], v[8:9]
	v_pk_add_f32 v[6:7], v[2:3], v[6:7]
	s_nop 0
	global_store_dwordx4 v[0:1], v[6:9], off sc1
	s_nop 1
	ds_read_b128 v[6:9], v13 offset:6528
	v_mad_i64_i32 v[0:1], s[2:3], v19, s0, 0
	v_lshl_add_u64 v[0:1], v[0:1], 2, s[8:9]
	v_lshl_add_u64 v[0:1], v[0:1], 0, v[10:11]
	s_waitcnt lgkmcnt(0)
	v_pk_add_f32 v[8:9], v[4:5], v[8:9]
	v_pk_add_f32 v[6:7], v[2:3], v[6:7]
	s_nop 0
	global_store_dwordx4 v[0:1], v[6:9], off sc1
	s_nop 1
	ds_read_b128 v[6:9], v13 offset:7616
	v_mad_i64_i32 v[0:1], s[0:1], v12, s0, 0
	v_lshl_add_u64 v[0:1], v[0:1], 2, s[8:9]
	v_lshl_add_u64 v[0:1], v[0:1], 0, v[10:11]
	s_waitcnt lgkmcnt(0)
	v_pk_add_f32 v[4:5], v[4:5], v[8:9]
	v_pk_add_f32 v[2:3], v[2:3], v[6:7]
	s_nop 0
	global_store_dwordx4 v[0:1], v[2:5], off sc1
	s_nop 1
	s_endpgm

amdhsa.kernels:
  - .agpr_count:     0
    .args:
      - .address_space:  global
        .offset:         0
        .size:           8
        .value_kind:     global_buffer
      - .address_space:  global
        .offset:         8
        .size:           8
        .value_kind:     global_buffer
      - .address_space:  global
        .offset:         16
        .size:           8
        .value_kind:     global_buffer
      - .address_space:  global
        .offset:         24
        .size:           8
        .value_kind:     global_buffer
      - .address_space:  global
        .offset:         32
        .size:           8
        .value_kind:     global_buffer
      - .address_space:  global
        .offset:         40
        .size:           8
        .value_kind:     global_buffer
      - .address_space:  global
        .offset:         48
        .size:           8
        .value_kind:     global_buffer
      - .address_space:  global
        .offset:         56
        .size:           8
        .value_kind:     global_buffer
    .group_segment_fixed_size: 0
    .kernarg_segment_align: 8
    .kernarg_segment_size: 64
    .language:       OpenCL C
    .language_version:
      - 2
      - 0
    .max_flat_workgroup_size: 256
    .name:           _Z10cvt_kernelPKfS0_S0_S0_S0_PDF16_S1_S1_
    .private_segment_fixed_size: 0
    .sgpr_count:     20
    .sgpr_spill_count: 0
    .symbol:         _Z10cvt_kernelPKfS0_S0_S0_S0_PDF16_S1_S1_.kd
    .uniform_work_group_size: 1
    .uses_dynamic_stack: false
    .vgpr_count:     70
    .vgpr_spill_count: 0
    .wavefront_size: 64
  - .agpr_count:     0
    .args:
      - .address_space:  global
        .offset:         0
        .size:           8
        .value_kind:     global_buffer
      - .address_space:  global
        .offset:         8
        .size:           8
        .value_kind:     global_buffer
      - .address_space:  global
        .offset:         16
        .size:           8
        .value_kind:     global_buffer
      - .address_space:  global
        .offset:         24
        .size:           8
        .value_kind:     global_buffer
    .group_segment_fixed_size: 2048
    .kernarg_segment_align: 8
    .kernarg_segment_size: 32
    .language:       OpenCL C
    .language_version:
      - 2
      - 0
    .max_flat_workgroup_size: 512
    .name:           _Z10attn64_fwdPKDF16_S0_S0_PDF16_
    .private_segment_fixed_size: 0
    .sgpr_count:     57
    .sgpr_spill_count: 0
    .symbol:         _Z10attn64_fwdPKDF16_S0_S0_PDF16_.kd
    .uniform_work_group_size: 1
    .uses_dynamic_stack: false
    .vgpr_count:     219
    .vgpr_spill_count: 0
    .wavefront_size: 64
  - .agpr_count:     0
    .args:
      - .address_space:  global
        .offset:         0
        .size:           8
        .value_kind:     global_buffer
      - .address_space:  global
        .offset:         8
        .size:           8
        .value_kind:     global_buffer
      - .address_space:  global
        .offset:         16
        .size:           8
        .value_kind:     global_buffer
      - .actual_access:  read_only
        .address_space:  global
        .offset:         24
        .size:           8
        .value_kind:     global_buffer
      - .offset:         32
        .size:           4
        .value_kind:     by_value
    .group_segment_fixed_size: 0
    .kernarg_segment_align: 8
    .kernarg_segment_size: 36
    .language:       OpenCL C
    .language_version:
      - 2
      - 0
    .max_flat_workgroup_size: 512
    .name:           _Z8gemm16_kILi256ELi192ELi0ELi2EEvPKDF16_S1_PvPKfi
    .private_segment_fixed_size: 0
    .sgpr_count:     30
    .sgpr_spill_count: 0
    .symbol:         _Z8gemm16_kILi256ELi192ELi0ELi2EEvPKDF16_S1_PvPKfi.kd
    .uniform_work_group_size: 1
    .uses_dynamic_stack: false
    .vgpr_count:     208
    .vgpr_spill_count: 0
    .wavefront_size: 64
  - .agpr_count:     0
    .args:
      - .address_space:  global
        .offset:         0
        .size:           8
        .value_kind:     global_buffer
      - .address_space:  global
        .offset:         8
        .size:           8
        .value_kind:     global_buffer
      - .address_space:  global
        .offset:         16
        .size:           8
        .value_kind:     global_buffer
      - .actual_access:  read_only
        .address_space:  global
        .offset:         24
        .size:           8
        .value_kind:     global_buffer
      - .offset:         32
        .size:           4
        .value_kind:     by_value
    .group_segment_fixed_size: 0
    .kernarg_segment_align: 8
    .kernarg_segment_size: 36
    .language:       OpenCL C
    .language_version:
      - 2
      - 0
    .max_flat_workgroup_size: 512
    .name:           _Z8gemm16_kILi128ELi128ELi1ELi3EEvPKDF16_S1_PvPKfi
    .private_segment_fixed_size: 0
    .sgpr_count:     28
    .sgpr_spill_count: 0
    .symbol:         _Z8gemm16_kILi128ELi128ELi1ELi3EEvPKDF16_S1_PvPKfi.kd
    .uniform_work_group_size: 1
    .uses_dynamic_stack: false
    .vgpr_count:     104
    .vgpr_spill_count: 0
    .wavefront_size: 64
